# split barriers: scan pass1->pass2 and Fourier stage C->out-projection posted mid-phase on own counters; full barrier completion deferred (stage A X loads / K-loop trip staging the recurrent half)
# speedup vs baseline: 1.0311x; 1.0053x over previous
.LBB0_367:
	v_readlane_b32 s46, v235, 14
	v_readlane_b32 s47, v235, 15
	s_mov_b32 s99, 0
	s_waitcnt vmcnt(0)
	s_barrier
	v_readfirstlane_b32 s100, v186
	s_nop 0
	s_cmp_lg_u32 s100, 0
	s_cbranch_scc1 .Lsc1_post_skip
	v_readlane_b32 s99, v235, 9
	v_readlane_b32 s100, v235, 7
	v_readlane_b32 s101, v235, 8
	s_lshl_b32 s99, s99, 8
	s_addk_i32 s99, 0x1c00
	v_mov_b32_e32 v236, s99
	v_mov_b32_e32 v237, 1
	s_mov_b64 exec, 1
	s_nop 1
	global_atomic_add v238, v236, v237, s[100:101] sc0
	s_mov_b64 exec, -1
	s_mov_b32 s99, 1
.Lsc1_post_skip:
.LBB0_368:
	v_mov_b32_e32 v0, v186
	s_and_b64 vcc, exec, s[6:7]
	s_cbranch_vccnz .LBB0_373
	v_lshlrev_b32_e32 v2, 4, v0
	v_and_b32_e32 v2, 0xf0, v2
	v_mov_b32_e32 v3, 0
	s_waitcnt lgkmcnt(0)
	v_lshl_add_u64 v[4:5], s[2:3], 0, v[2:3]
	s_mov_b64 s[0:1], 0xa7b000
	v_bfe_u32 v9, v0, 4, 2
	v_lshl_add_u64 v[32:33], v[4:5], 0, s[0:1]
	v_ashrrev_i32_e32 v4, 2, v0
	v_and_b32_e32 v1, 15, v0
	v_and_b32_e32 v11, -16, v4
	v_bfi_b32 v38, -16, v4, v0
	v_lshlrev_b32_e32 v4, 4, v9
	v_mov_b32_e32 v5, v3
	v_lshl_add_u64 v[6:7], s[2:3], 0, v[4:5]
	v_add_u32_e32 v5, 0, v2
	v_lshlrev_b32_e32 v2, 2, v1
	v_lshl_add_u64 v[2:3], s[2:3], 0, v[2:3]
	s_mov_b64 s[2:3], 0x112f3000
	v_lshl_add_u64 v[36:37], v[2:3], 0, s[2:3]
	v_lshlrev_b32_e32 v3, 2, v0
	v_ashrrev_i32_e32 v2, 11, v0
	v_and_b32_e32 v3, 0x1fc0, v3
	s_mov_b64 s[0:1], 0x1a7b000
	v_add_u32_e32 v41, v3, v2
	v_add_u32_e32 v2, 0x200, v0
	v_bfe_u32 v10, v0, 4, 4
	v_lshl_add_u64 v[34:35], v[6:7], 0, s[0:1]
	v_ashrrev_i32_e32 v6, 11, v2
	v_lshrrev_b32_e32 v2, 4, v2
	s_movk_i32 s0, 0x70
	v_and_or_b32 v7, v2, s0, v10
	v_lshl_add_u32 v42, v7, 6, v6
	v_add_u32_e32 v6, 0x400, v0
	v_ashrrev_i32_e32 v7, 11, v6
	v_lshrrev_b32_e32 v6, 4, v6
	v_lshl_or_b32 v40, v9, 2, v11
	v_and_or_b32 v9, v6, s0, v10
	v_lshl_add_u32 v43, v9, 6, v7
	v_add_u32_e32 v7, 0x600, v0
	v_ashrrev_i32_e32 v9, 11, v7
	v_lshrrev_b32_e32 v7, 4, v7
	v_and_or_b32 v11, v7, s0, v10
	v_lshl_add_u32 v44, v11, 6, v9
	v_add_u32_e32 v9, 0x800, v0
	v_ashrrev_i32_e32 v11, 11, v9
	v_add_u32_e32 v45, v3, v11
	v_add_u32_e32 v3, 0xa00, v0
	v_ashrrev_i32_e32 v11, 11, v3
	v_lshrrev_b32_e32 v3, 4, v3
	v_and_or_b32 v12, v3, s0, v10
	v_lshl_add_u32 v46, v12, 6, v11
	v_add_u32_e32 v11, 0xc00, v0
	v_ashrrev_i32_e32 v12, 11, v11
	v_lshrrev_b32_e32 v11, 4, v11
	v_lshrrev_b32_e32 v8, 4, v0
	v_and_or_b32 v13, v11, s0, v10
	v_add_u32_e32 v0, 0xe00, v0
	v_lshl_add_u32 v47, v13, 6, v12
	v_ashrrev_i32_e32 v12, 11, v0
	v_lshrrev_b32_e32 v0, 4, v0
	v_and_or_b32 v10, v0, s0, v10
	s_movk_i32 s0, 0x110
	v_lshrrev_b32_e32 v9, 4, v9
	v_lshl_add_u32 v48, v10, 6, v12
	v_mul_lo_u32 v8, v8, s0
	v_mul_lo_u32 v2, v2, s0
	v_mul_lo_u32 v6, v6, s0
	v_mul_lo_u32 v7, v7, s0
	v_mul_lo_u32 v9, v9, s0
	v_mul_lo_u32 v3, v3, s0
	v_mul_lo_u32 v10, v11, s0
	v_mul_lo_u32 v0, v0, s0
	v_mul_u32_u24_e32 v1, 0x110, v1
	v_readlane_b32 s2, v235, 16
	v_add_u32_e32 v39, 0x80, v38
	s_mov_b32 s1, 0
	v_add3_u32 v49, v1, v4, 0
	v_add_u32_e32 v50, v5, v8
	v_add_u32_e32 v51, v5, v2
	v_add_u32_e32 v52, v5, v6
	v_add_u32_e32 v53, v5, v7
	v_add_u32_e32 v54, v5, v9
	v_add_u32_e32 v55, v5, v3
	v_add_u32_e32 v56, v5, v10
	v_add_u32_e32 v57, v5, v0
	s_mov_b32 s8, s2
	v_readlane_b32 s3, v235, 17
.LBB0_370:
	s_bfe_u32 s9, s8, 0x10005
	s_lshl_b32 s2, s8, 1
	s_and_b32 s10, s2, 62
	s_lshl_b32 s2, s9, 13
	s_ashr_i32 s0, s8, 6
	s_or_b32 s11, s2, s10
	s_lshl_b32 s2, s0, 7
	v_add_u32_e32 v2, s11, v41
	v_add_u32_e32 v4, s11, v42
	s_ashr_i32 s3, s2, 31
	v_ashrrev_i32_e32 v3, 31, v2
	v_ashrrev_i32_e32 v5, 31, v4
	v_lshl_add_u64 v[0:1], s[2:3], 1, v[32:33]
	v_lshlrev_b64 v[2:3], 10, v[2:3]
	v_lshlrev_b64 v[4:5], 10, v[4:5]
	v_lshl_add_u64 v[2:3], v[0:1], 0, v[2:3]
	v_lshl_add_u64 v[4:5], v[0:1], 0, v[4:5]
	global_load_dwordx4 v[60:63], v[2:3], off
	global_load_dwordx4 v[64:67], v[4:5], off
	v_add_u32_e32 v2, s11, v43
	v_add_u32_e32 v4, s11, v44
	v_ashrrev_i32_e32 v3, 31, v2
	v_ashrrev_i32_e32 v5, 31, v4
	v_lshlrev_b64 v[2:3], 10, v[2:3]
	v_lshlrev_b64 v[4:5], 10, v[4:5]
	v_lshl_add_u64 v[2:3], v[0:1], 0, v[2:3]
	v_lshl_add_u64 v[4:5], v[0:1], 0, v[4:5]
	global_load_dwordx4 v[68:71], v[2:3], off
	global_load_dwordx4 v[72:75], v[4:5], off
	v_add_u32_e32 v2, s11, v45
	v_add_u32_e32 v4, s11, v46
	v_ashrrev_i32_e32 v3, 31, v2
	v_ashrrev_i32_e32 v5, 31, v4
	v_lshlrev_b64 v[2:3], 10, v[2:3]
	v_lshlrev_b64 v[4:5], 10, v[4:5]
	v_lshl_add_u64 v[2:3], v[0:1], 0, v[2:3]
	v_lshl_add_u64 v[4:5], v[0:1], 0, v[4:5]
	global_load_dwordx4 v[76:79], v[2:3], off
	global_load_dwordx4 v[80:83], v[4:5], off
	v_add_u32_e32 v2, s11, v47
	v_add_u32_e32 v4, s11, v48
	v_ashrrev_i32_e32 v3, 31, v2
	v_ashrrev_i32_e32 v5, 31, v4
	v_lshlrev_b64 v[2:3], 10, v[2:3]
	v_lshlrev_b64 v[4:5], 10, v[4:5]
	v_lshl_add_u64 v[2:3], v[0:1], 0, v[2:3]
	v_lshl_add_u64 v[0:1], v[0:1], 0, v[4:5]
	s_lshl_b32 s0, s0, 8
	global_load_dwordx4 v[84:87], v[2:3], off
	global_load_dwordx4 v[88:91], v[0:1], off
	v_add_u32_e32 v0, s0, v38
	v_ashrrev_i32_e32 v1, 31, v0
	v_lshlrev_b64 v[0:1], 8, v[0:1]
	v_lshl_add_u64 v[58:59], v[34:35], 0, v[0:1]
	v_add_u32_e32 v0, s0, v39
	v_ashrrev_i32_e32 v1, 31, v0
	v_lshlrev_b64 v[0:1], 8, v[0:1]
	v_lshl_add_u64 v[92:93], v[34:35], 0, v[0:1]
	global_load_dwordx4 v[0:3], v[58:59], off
	global_load_dwordx4 v[4:7], v[58:59], off offset:64
	global_load_dwordx4 v[8:11], v[92:93], off
	global_load_dwordx4 v[12:15], v[92:93], off offset:64
	global_load_dwordx4 v[16:19], v[58:59], off offset:128
	global_load_dwordx4 v[20:23], v[58:59], off offset:192
	global_load_dwordx4 v[24:27], v[92:93], off offset:128
	global_load_dwordx4 v[28:31], v[92:93], off offset:192
	s_lshl_b32 s0, s9, 6
	s_mov_b32 s3, s1
	v_mov_b32_e32 v58, v49
	s_or_b32 s9, s0, s10
	v_add_u32_e32 v59, s2, v40
	s_mov_b32 s2, s1
	s_waitcnt vmcnt(63) expcnt(7) lgkmcnt(15)
	s_barrier
	s_waitcnt vmcnt(15)
	ds_write_b128 v50, v[60:63]
	s_waitcnt vmcnt(14)
	ds_write_b128 v51, v[64:67]
	s_waitcnt vmcnt(13)
	ds_write_b128 v52, v[68:71]
	s_waitcnt vmcnt(12)
	ds_write_b128 v53, v[72:75]
	s_waitcnt vmcnt(11)
	ds_write_b128 v54, v[76:79]
	s_waitcnt vmcnt(10)
	ds_write_b128 v55, v[80:83]
	s_waitcnt vmcnt(9)
	ds_write_b128 v56, v[84:87]
	s_waitcnt vmcnt(8)
	ds_write_b128 v57, v[88:91]
	s_waitcnt lgkmcnt(0)
	s_barrier
	s_waitcnt vmcnt(0)
	s_cmp_eq_u32 s99, 0
	s_cbranch_scc1 .Lsc1_chk_skip
	s_mov_b32 s99, 0
	v_mov_b32_e32 v239, 0x20000
	ds_read_b32 v239, v239
	v_add_u32_e32 v238, 1, v238
	s_waitcnt lgkmcnt(0)
	v_readfirstlane_b32 s100, v238
	v_readfirstlane_b32 s101, v239
	s_nop 0
	s_cmp_lg_u32 s100, s101
	s_cbranch_scc1 .Lsc1_chk_skip
	buffer_wbl2 sc1
	s_waitcnt vmcnt(0)
	v_readlane_b32 s100, v235, 7
	v_readlane_b32 s101, v235, 8
	v_mov_b32_e32 v236, 0x2c00
	v_mov_b32_e32 v237, 1
	s_mov_b64 exec, 1
	s_nop 3
	global_atomic_add v236, v237, s[100:101]
	s_mov_b64 exec, -1
.Lsc1_chk_skip:
.LBB0_371:
	ds_read_b128 v[60:63], v58
	ds_read_b128 v[64:67], v58 offset:64
	ds_read_b128 v[72:75], v58 offset:4352
	ds_read_b128 v[76:79], v58 offset:4416
	ds_read_b128 v[84:87], v58 offset:128
	ds_read_b128 v[88:91], v58 offset:192
	s_waitcnt lgkmcnt(5)
	v_mfma_f32_16x16x32_bf16 v[68:71], v[0:3], v[60:63], 0
	ds_read_b128 v[92:95], v58 offset:4480
	ds_read_b128 v[96:99], v58 offset:4544
	s_lshr_b32 s0, s2, 3
	s_add_i32 s12, s9, s0
	v_mfma_f32_16x16x32_bf16 v[60:63], v[8:11], v[60:63], 0
	s_and_b32 s10, s3, 0x60
	s_add_i32 s11, s3, 16
	s_lshl_b32 s0, s10, 2
	s_waitcnt lgkmcnt(5)
	v_mfma_f32_16x16x32_bf16 v[80:83], v[0:3], v[72:75], 0
	s_and_b32 s10, s11, 0x70
	s_add_i32 s2, s2, 2
	s_add_i32 s3, s3, 32
	v_mfma_f32_16x16x32_bf16 v[72:75], v[8:11], v[72:75], 0
	v_add_u32_e32 v58, 0x2200, v58
	v_mfma_f32_16x16x32_bf16 v[68:71], v[4:7], v[64:67], v[68:71]
	v_mfma_f32_16x16x32_bf16 v[60:63], v[12:15], v[64:67], v[60:63]
	s_waitcnt lgkmcnt(4)
	v_mfma_f32_16x16x32_bf16 v[64:67], v[4:7], v[76:79], v[80:83]
	v_mfma_f32_16x16x32_bf16 v[72:75], v[12:15], v[76:79], v[72:75]
	v_lshl_add_u32 v76, s12, 9, v59
	v_ashrrev_i32_e32 v77, 31, v76
	v_or_b32_e32 v80, 1, v76
	s_waitcnt lgkmcnt(3)
	v_mfma_f32_16x16x32_bf16 v[68:71], v[16:19], v[84:87], v[68:71]
	v_or_b32_e32 v82, 2, v76
	v_lshl_add_u64 v[78:79], v[36:37], 0, s[0:1]
	s_lshl_b32 s0, s10, 2
	v_mfma_f32_16x16x32_bf16 v[60:63], v[24:27], v[84:87], v[60:63]
	v_or_b32_e32 v84, 3, v76
	v_lshlrev_b64 v[76:77], 9, v[76:77]
	v_ashrrev_i32_e32 v81, 31, v80
	s_waitcnt lgkmcnt(1)
	v_mfma_f32_16x16x32_bf16 v[64:67], v[16:19], v[92:95], v[64:67]
	v_ashrrev_i32_e32 v83, 31, v82
	v_ashrrev_i32_e32 v85, 31, v84
	v_lshl_add_u64 v[86:87], v[36:37], 0, s[0:1]
	v_mfma_f32_16x16x32_bf16 v[72:75], v[24:27], v[92:95], v[72:75]
	s_cmp_eq_u32 s2, 16
	v_lshl_add_u64 v[92:93], v[78:79], 0, v[76:77]
	v_lshlrev_b64 v[80:81], 9, v[80:81]
	v_mfma_f32_16x16x32_bf16 v[68:71], v[20:23], v[88:91], v[68:71]
	v_lshlrev_b64 v[82:83], 9, v[82:83]
	v_lshlrev_b64 v[84:85], 9, v[84:85]
	v_lshl_add_u64 v[76:77], v[86:87], 0, v[76:77]
	v_mfma_f32_16x16x32_bf16 v[60:63], v[28:31], v[88:91], v[60:63]
	v_lshl_add_u64 v[88:89], v[78:79], 0, v[80:81]
	v_lshl_add_u64 v[90:91], v[78:79], 0, v[82:83]
	v_lshl_add_u64 v[78:79], v[78:79], 0, v[84:85]
	s_waitcnt lgkmcnt(0)
	v_mfma_f32_16x16x32_bf16 v[64:67], v[20:23], v[96:99], v[64:67]
	v_lshl_add_u64 v[80:81], v[86:87], 0, v[80:81]
	s_nop 1
	v_cvt_pk_bf16_f32 v60, v68, v60
	v_lshl_add_u64 v[82:83], v[86:87], 0, v[82:83]
	v_mfma_f32_16x16x32_bf16 v[72:75], v[28:31], v[96:99], v[72:75]
	v_lshl_add_u64 v[84:85], v[86:87], 0, v[84:85]
	v_cvt_pk_bf16_f32 v61, v69, v61
	v_cvt_pk_bf16_f32 v62, v70, v62
	v_cvt_pk_bf16_f32 v63, v71, v63
	s_nop 3
	v_cvt_pk_bf16_f32 v64, v64, v72
	v_cvt_pk_bf16_f32 v65, v65, v73
	v_cvt_pk_bf16_f32 v66, v66, v74
	v_cvt_pk_bf16_f32 v67, v67, v75
	global_store_dword v[92:93], v60, off
	global_store_dword v[88:89], v61, off
	global_store_dword v[90:91], v62, off
	global_store_dword v[78:79], v63, off
	global_store_dword v[76:77], v64, off
	global_store_dword v[80:81], v65, off
	global_store_dword v[82:83], v66, off
	global_store_dword v[84:85], v67, off
	s_cbranch_scc0 .LBB0_371
	v_readlane_b32 s12, v235, 0
	v_readlane_b32 s14, v235, 2
	s_add_i32 s8, s8, s14
	s_cmpk_gt_i32 s8, 0xff
	v_readlane_b32 s13, v235, 1
	v_readlane_b32 s15, v235, 3
	s_cbranch_scc0 .LBB0_370

.Lxb_poll_3:
	v_readfirstlane_b32 s98, v236
	v_mov_b32_e32 v237, 0x2c00
	v_mov_b32_e32 v239, 0
.Lsc3_poll:
	global_load_dword v238, v237, s[100:101] sc1
	s_waitcnt vmcnt(0)
	v_cmp_ge_u32_e32 vcc, v238, v0
	s_cbranch_vccnz .Lxb_done_3
	s_sleep 1
	v_add_u32_e32 v239, 1, v239
	v_cmp_gt_u32_e32 vcc, 0x8000, v239
	s_cbranch_vccnz .Lsc3_poll
	s_branch .Lxb_done_3

.LBB0_431:
	s_ashr_i32 s9, s15, 2
	s_and_b32 s9, s9, -16
	v_or_b32_e32 v130, s9, v140
	s_waitcnt vmcnt(15)
	v_mul_lo_u32 v64, v130, v141
	v_ashrrev_i32_e32 v65, 31, v64
	v_lshl_add_u64 v[66:67], v[64:65], 2, s[2:3]
	v_add_u32_e32 v65, 0x1800, v64
	v_and_b32_e32 v65, 0x1ffc, v65
	v_add_u32_e32 v64, v64, v130
	s_waitcnt vmcnt(13)
	v_lshlrev_b32_e32 v74, 2, v65
	v_ashrrev_i32_e32 v65, 31, v64
	v_lshl_add_u64 v[68:69], v[64:65], 2, s[2:3]
	v_add_u32_e32 v65, 0x1800, v64
	v_and_b32_e32 v65, 0x1fff, v65
	v_add_u32_e32 v64, v64, v130
	v_lshlrev_b32_e32 v75, 2, v65
	v_ashrrev_i32_e32 v65, 31, v64
	v_lshl_add_u64 v[70:71], v[64:65], 2, s[2:3]
	v_add_u32_e32 v65, 0x1800, v64
	v_and_b32_e32 v65, 0x1ffe, v65
	v_add_u32_e32 v64, v64, v130
	s_waitcnt vmcnt(12)
	v_lshlrev_b32_e32 v76, 2, v65
	v_ashrrev_i32_e32 v65, 31, v64
	v_lshl_add_u64 v[72:73], v[64:65], 2, s[2:3]
	v_add_u32_e32 v64, 0x1800, v64
	s_lshl_b32 s10, s15, 1
	v_and_b32_e32 v64, 0x1fff, v64
	s_and_b32 s10, s10, 64
	s_lshl_b32 s8, s15, 4
	v_lshlrev_b32_e32 v64, 2, v64
	s_add_i32 s10, s10, s9
	global_load_dword v98, v[66:67], off
	global_load_dword v100, v74, s[2:3]
	global_load_dword v102, v[68:69], off
	global_load_dword v104, v75, s[2:3]
	global_load_dword v106, v[70:71], off
	global_load_dword v108, v76, s[2:3]
	global_load_dword v110, v[72:73], off
	global_load_dword v112, v64, s[2:3]
	s_and_b32 s8, s8, 0x1f0
	v_or_b32_e32 v64, s10, v142
	v_lshl_or_b32 v99, v64, 9, s8
	v_add_u32_e32 v64, v99, v143
	v_ashrrev_i32_e32 v65, 31, v64
	v_lshlrev_b64 v[64:65], 9, v[64:65]
	v_lshl_add_u64 v[72:73], v[96:97], 0, v[64:65]
	v_add_u32_e32 v64, v99, v144
	v_ashrrev_i32_e32 v65, 31, v64
	v_lshlrev_b64 v[64:65], 9, v[64:65]
	v_lshl_add_u64 v[74:75], v[96:97], 0, v[64:65]
	v_readfirstlane_b32 s100, v186
	s_nop 0
	s_cmp_lg_u32 s100, 0
	s_cbranch_scc1 .Ldfa_w_skip
	s_cmp_eq_u32 s98, 0
	s_cbranch_scc1 .Ldfa_w_skip
	v_readlane_b32 s100, v235, 7
	v_readlane_b32 s101, v235, 8
	v_mov_b32_e32 v236, 0x3400
	v_mov_b32_e32 v239, 0
	s_nop 3
.Ldfa_w_poll:
	global_load_dword v237, v236, s[100:101] sc1
	s_waitcnt vmcnt(0)
	v_readfirstlane_b32 s99, v237
	s_nop 0
	s_cmp_ge_u32 s99, s98
	s_cbranch_scc1 .Ldfa_w_ok
	s_sleep 1
	v_add_u32_e32 v239, 1, v239
	v_readfirstlane_b32 s99, v239
	s_nop 0
	s_cmp_lt_u32 s99, 0x8000
	s_cbranch_scc1 .Ldfa_w_poll

.Ldfa_w_skip:
	s_barrier
	global_load_dwordx4 v[64:67], v[72:73], off
	global_load_dwordx4 v[68:71], v[74:75], off
	v_add_u32_e32 v72, v99, v145
	v_ashrrev_i32_e32 v73, 31, v72
	v_lshlrev_b64 v[72:73], 9, v[72:73]
	s_waitcnt vmcnt(21)
	v_lshl_add_u64 v[80:81], v[96:97], 0, v[72:73]
	v_add_u32_e32 v72, v99, v146
	v_ashrrev_i32_e32 v73, 31, v72
	v_lshlrev_b64 v[72:73], 9, v[72:73]
	v_lshl_add_u64 v[82:83], v[96:97], 0, v[72:73]
	global_load_dwordx4 v[72:75], v[80:81], off
	global_load_dwordx4 v[76:79], v[82:83], off
	v_add_u32_e32 v80, v99, v147
	v_add_u32_e32 v82, v99, v148
	s_waitcnt vmcnt(21)
	v_add_u32_e32 v88, v99, v149
	v_add_u32_e32 v90, v99, v150
	v_ashrrev_i32_e32 v81, 31, v80
	v_ashrrev_i32_e32 v83, 31, v82
	v_ashrrev_i32_e32 v89, 31, v88
	v_ashrrev_i32_e32 v91, 31, v90
	v_lshlrev_b64 v[80:81], 9, v[80:81]
	v_lshlrev_b64 v[82:83], 9, v[82:83]
	v_lshlrev_b64 v[88:89], 9, v[88:89]
	v_lshlrev_b64 v[90:91], 9, v[90:91]
	v_lshl_add_u64 v[80:81], v[96:97], 0, v[80:81]
	v_lshl_add_u64 v[84:85], v[96:97], 0, v[82:83]
	v_lshl_add_u64 v[88:89], v[96:97], 0, v[88:89]
	s_waitcnt vmcnt(20)
	v_lshl_add_u64 v[92:93], v[96:97], 0, v[90:91]
	global_load_dwordx4 v[80:83], v[80:81], off
	s_nop 0
	global_load_dwordx4 v[84:87], v[84:85], off
	s_nop 0
	global_load_dwordx4 v[88:91], v[88:89], off
	s_nop 0
	global_load_dwordx4 v[92:95], v[92:93], off
	v_or_b32_e32 v99, 8, v99
	s_lshl_b32 s8, s15, 11
	v_add_u32_e32 v114, v99, v143
	v_add_u32_e32 v116, v99, v144
	v_add_u32_e32 v118, v99, v145
	v_add_u32_e32 v120, v99, v146
	v_add_u32_e32 v122, v99, v147
	v_add_u32_e32 v124, v99, v148
	v_add_u32_e32 v126, v99, v149
	v_add_u32_e32 v128, v99, v150
	s_and_b32 s8, s8, 0x10000
	s_and_b32 s9, s12, 0x1f0
	v_ashrrev_i32_e32 v115, 31, v114
	v_ashrrev_i32_e32 v117, 31, v116
	v_ashrrev_i32_e32 v119, 31, v118
	v_ashrrev_i32_e32 v121, 31, v120
	v_ashrrev_i32_e32 v123, 31, v122
	v_ashrrev_i32_e32 v125, 31, v124
	v_ashrrev_i32_e32 v127, 31, v126
	v_ashrrev_i32_e32 v129, 31, v128
	v_ashrrev_i32_e32 v131, 31, v130
	v_lshlrev_b64 v[114:115], 9, v[114:115]
	v_lshlrev_b64 v[116:117], 9, v[116:117]
	v_lshlrev_b64 v[118:119], 9, v[118:119]
	v_lshlrev_b64 v[120:121], 9, v[120:121]
	v_lshlrev_b64 v[122:123], 9, v[122:123]
	v_lshlrev_b64 v[124:125], 9, v[124:125]
	v_lshlrev_b64 v[126:127], 9, v[126:127]
	v_lshlrev_b64 v[128:129], 9, v[128:129]
	s_or_b32 s8, s9, s8
	v_lshl_add_u64 v[114:115], v[96:97], 0, v[114:115]
	v_lshl_add_u64 v[116:117], v[96:97], 0, v[116:117]
	v_lshl_add_u64 v[118:119], v[96:97], 0, v[118:119]
	v_lshl_add_u64 v[120:121], v[96:97], 0, v[120:121]
	v_lshl_add_u64 v[122:123], v[96:97], 0, v[122:123]
	v_lshl_add_u64 v[124:125], v[96:97], 0, v[124:125]
	v_lshl_add_u64 v[126:127], v[96:97], 0, v[126:127]
	v_lshl_add_u64 v[128:129], v[96:97], 0, v[128:129]
	s_waitcnt vmcnt(15)
	v_mov_b32_e32 v99, v98
	s_waitcnt vmcnt(14)
	v_mov_b32_e32 v101, v100
	s_waitcnt vmcnt(13)
	v_mov_b32_e32 v103, v102
	s_waitcnt vmcnt(12)
	v_mov_b32_e32 v105, v104
	s_waitcnt vmcnt(11)
	v_mov_b32_e32 v107, v106
	s_waitcnt vmcnt(10)
	v_mov_b32_e32 v109, v108
	s_waitcnt vmcnt(9)
	v_mov_b32_e32 v111, v110
	s_waitcnt vmcnt(8)
	v_mov_b32_e32 v113, v112
	v_lshl_add_u64 v[130:131], v[130:131], 2, s[0:1]
	v_add_u32_e32 v164, s8, v153
	v_add_u32_e32 v165, s8, v154
	v_add_u32_e32 v166, s8, v155
	v_add_u32_e32 v167, s8, v152
	s_mov_b64 s[10:11], -1
	s_mov_b32 s16, 0

.LBB0_494:
	v_writelane_b32 v235, s20, 19
	s_or_b64 exec, exec, s[2:3]
	s_mov_b32 s99, 0
	s_waitcnt vmcnt(0)
	s_barrier
	v_readfirstlane_b32 s100, v186
	s_nop 0
	s_cmp_lg_u32 s100, 0
	s_cbranch_scc1 .Lsc2_post_skip
	v_readlane_b32 s99, v235, 9
	v_readlane_b32 s100, v235, 7
	v_readlane_b32 s101, v235, 8
	s_lshl_b32 s99, s99, 8
	s_addk_i32 s99, 0x1c80
	v_mov_b32_e32 v236, s99
	v_mov_b32_e32 v237, 1
	s_mov_b64 exec, 1
	s_nop 1
	global_atomic_add v238, v236, v237, s[100:101] sc0
	s_mov_b64 exec, -1
	s_mov_b32 s99, 1
.Lsc2_post_skip:
	v_mov_b32_e32 v0, v186
	s_and_b64 vcc, exec, s[6:7]
	s_cbranch_vccnz .LBB0_499
	v_and_b32_e32 v3, 63, v0
	s_load_dwordx2 s[14:15], s[14:15], 0x50
	v_mov_b32_e32 v123, 0
	v_lshlrev_b32_e32 v122, 1, v3
	v_lshlrev_b32_e32 v2, 4, v0
	s_waitcnt lgkmcnt(0)
	v_lshl_add_u64 v[6:7], s[0:1], 0, v[122:123]
	s_mov_b64 s[16:17], 0x166f3000
	v_and_b32_e32 v1, 15, v0
	v_and_b32_e32 v120, 0x70, v2
	v_lshl_add_u64 v[124:125], v[6:7], 0, s[16:17]
	v_mbcnt_hi_u32_b32 v7, -1, v187
	v_ashrrev_i32_e32 v121, 6, v0
	v_ashrrev_i32_e32 v135, 3, v0
	v_ashrrev_i32_e32 v152, 4, v0
	v_lshlrev_b32_e32 v2, 2, v120
	v_lshl_add_u32 v8, v1, 2, 0
	v_bfe_u32 v9, v0, 4, 2
	v_mov_b32_e32 v3, v123
	v_and_b32_e32 v0, 0xffffffc0, v0
	v_and_b32_e32 v10, 64, v7
	v_add_u32_e32 v5, 0, v2
	v_lshl_add_u64 v[126:127], s[14:15], 0, v[2:3]
	v_mad_u32_u24 v2, v1, 12, v8
	v_add_u32_e32 v0, v8, v0
	v_xor_b32_e32 v8, 1, v7
	v_add_u32_e32 v10, 64, v10
	v_cmp_lt_i32_e32 vcc, v8, v10
	s_add_u32 s2, s0, 0xf1f3000
	s_addc_u32 s3, s1, 0
	v_cndmask_b32_e32 v8, v7, v8, vcc
	v_lshlrev_b32_e32 v153, 2, v8
	v_xor_b32_e32 v8, 2, v7
	v_cmp_lt_i32_e32 vcc, v8, v10
	s_add_u32 s6, s0, 0xe173000
	s_addc_u32 s7, s1, 0
	v_cndmask_b32_e32 v8, v7, v8, vcc
	v_lshlrev_b32_e32 v154, 2, v8
	v_xor_b32_e32 v8, 4, v7
	s_add_u32 s8, s0, 0x1771b000
	s_movk_i32 s12, 0x210
	v_cmp_lt_i32_e32 vcc, v8, v10
	s_addc_u32 s9, s1, 0
	v_lshlrev_b32_e32 v3, 3, v9
	v_mul_lo_u32 v6, v135, s12
	v_cndmask_b32_e32 v7, v7, v8, vcc
	s_movk_i32 s12, 0x110
	v_mul_u32_u24_e32 v8, 0x110, v1
	v_readlane_b32 s20, v235, 0
	s_add_u32 s10, s0, 0x1871b000
	v_lshlrev_b32_e32 v4, 3, v1
	v_lshlrev_b32_e32 v155, 2, v7
	v_mul_lo_u32 v7, v152, s12
	v_add3_u32 v156, 0, v3, v8
	v_mul_u32_u24_e32 v3, 0x840, v9
	v_lshlrev_b32_e32 v122, 4, v1
	v_readlane_b32 s26, v235, 16
	v_readlane_b32 s21, v235, 1
	v_readlane_b32 s22, v235, 2
	v_readlane_b32 s23, v235, 3
	s_addc_u32 s11, s1, 0
	s_mov_b32 s13, 0
	v_add_u32_e32 v157, 0x400, v121
	v_lshl_add_u64 v[128:129], s[2:3], 0, v[122:123]
	s_lshl_b32 s18, s26, 8
	s_lshl_b32 s19, s22, 8
	v_lshlrev_b32_e32 v130, 1, v4
	v_mov_b32_e32 v131, v123
	s_mov_b64 s[14:15], 0x10000
	s_mov_b32 s20, 0x10000
	v_mov_b32_e32 v158, 0x358637bd
	s_mov_b32 s21, 0x800000
	s_mov_b64 s[16:17], 0x1971b400
	s_mov_b32 s22, 0x1971b000
	v_add_u32_e32 v159, v2, v7
	v_add_u32_e32 v160, v0, v3
	v_add_u32_e32 v161, v5, v6
	s_mov_b32 s23, s26
	v_readlane_b32 s27, v235, 17

.LBB0_497:
	v_add_u32_e32 v18, s26, v162
	v_add_u32_e32 v16, 64, v18
	v_add_u32_e32 v18, 0x60, v18
	v_ashrrev_i32_e32 v17, 31, v16
	v_ashrrev_i32_e32 v19, 31, v18
	v_lshlrev_b64 v[16:17], 11, v[16:17]
	v_lshlrev_b64 v[18:19], 11, v[18:19]
	v_lshl_add_u64 v[16:17], v[136:137], 0, v[16:17]
	v_lshl_add_u64 v[18:19], v[136:137], 0, v[18:19]
	v_add_u32_e32 v138, s26, v133
	ds_write_b128 v159, v[52:55]
	ds_write_b128 v159, v[64:67] offset:8704
	ds_write_b128 v159, v[56:59] offset:17408
	ds_write_b128 v159, v[60:63] offset:26112
	s_waitcnt lgkmcnt(0)
	s_barrier
	s_cmp_eq_u32 s99, 0
	s_cbranch_scc1 .Lsc2_chk_skip
	s_mov_b32 s99, 0
	s_waitcnt vmcnt(0)
	v_mov_b32_e32 v239, 0x20000
	ds_read_b32 v239, v239
	v_add_u32_e32 v238, 1, v238
	s_waitcnt lgkmcnt(0)
	v_readfirstlane_b32 s100, v238
	v_readfirstlane_b32 s101, v239
	s_nop 0
	s_cmp_lg_u32 s100, s101
	s_cbranch_scc1 .Lsc2_chk_skip
	buffer_wbl2 sc1
	s_waitcnt vmcnt(0)
	v_readlane_b32 s100, v235, 7
	v_readlane_b32 s101, v235, 8
	v_mov_b32_e32 v236, 0x2c80
	v_mov_b32_e32 v237, 1
	s_mov_b64 exec, 1
	s_nop 3
	global_atomic_add v236, v237, s[100:101]
	s_mov_b64 exec, -1
.Lsc2_chk_skip:
	global_load_dwordx4 v[52:55], v[16:17], off nt
	global_load_dwordx4 v[64:67], v[18:19], off nt
	global_load_dwordx4 v[56:59], v[16:17], off offset:1024 nt
	global_load_dwordx4 v[60:63], v[18:19], off offset:1024 nt
	v_add_u32_e32 v16, 64, v138
	v_ashrrev_i32_e32 v17, 31, v16
	v_lshlrev_b64 v[16:17], 10, v[16:17]
	v_lshl_or_b32 v16, v134, 1, v16
	v_lshl_add_u64 v[18:19], s[8:9], 0, v[16:17]
	global_load_dwordx4 v[40:43], v[18:19], off offset:16 nt
	global_load_dwordx4 v[24:27], v[18:19], off nt
	v_lshl_add_u64 v[18:19], s[10:11], 0, v[16:17]
	v_lshl_add_u64 v[16:17], s[6:7], 0, v[16:17]
	global_load_dwordx4 v[32:35], v[18:19], off offset:16 nt
	global_load_dwordx4 v[20:23], v[18:19], off nt
	global_load_dwordx4 v[36:39], v[16:17], off offset:16 nt
	s_nop 0
	global_load_dwordx4 v[16:19], v[16:17], off nt
	ds_read2_b64 v[112:115], v156 offset1:4
	ds_read2_b64 v[148:151], v156 offset0:8 offset1:12
	v_add_u32_e32 v163, 0x1000, v156
	s_waitcnt lgkmcnt(1)
	v_mfma_f32_16x16x32_bf16 v[112:115], v[112:115], v[84:87], 0
	ds_read2_b64 v[116:119], v163 offset0:32 offset1:36
	v_add_u32_e32 v164, 0x2000, v156
	ds_read2_b64 v[140:143], v164 offset0:64 offset1:68
	s_waitcnt lgkmcnt(2)
	v_mfma_f32_16x16x32_bf16 v[112:115], v[148:151], v[80:83], v[112:115]
	ds_read2_b64 v[148:151], v163 offset0:40 offset1:44
	v_add_u32_e32 v165, 0x3000, v156
	ds_read2_b64 v[144:147], v165 offset0:96 offset1:100
	s_waitcnt lgkmcnt(3)
	v_mfma_f32_16x16x32_bf16 v[116:119], v[116:119], v[84:87], 0
	v_add_u32_e32 v166, 0x4000, v156
	v_add_u32_e32 v167, 0x5000, v156
	v_add_u32_e32 v168, 0x6000, v156
	s_waitcnt lgkmcnt(1)
	v_mfma_f32_16x16x32_bf16 v[116:119], v[148:151], v[80:83], v[116:119]
	ds_read2_b64 v[148:151], v164 offset0:72 offset1:76
	v_add_u32_e32 v169, 0x7000, v156
	v_add_u32_e32 v170, 0x8800, v160
	v_mfma_f32_16x16x32_bf16 v[140:143], v[140:143], v[84:87], 0
	v_add_u32_e32 v171, 0x8c00, v160
	v_add_u32_e32 v172, 0xa800, v160
	v_add_u32_e32 v173, 0xac00, v160
	s_waitcnt lgkmcnt(0)
	v_mfma_f32_16x16x32_bf16 v[140:143], v[148:151], v[80:83], v[140:143]
	ds_read2_b64 v[148:151], v165 offset0:104 offset1:108
	v_add_u32_e32 v174, 0xca00, v160
	v_add_u32_e32 v175, 0xce00, v160
	v_mfma_f32_16x16x32_bf16 v[144:147], v[144:147], v[84:87], 0
	v_add_u32_e32 v176, 0xea00, v160
	v_add_u32_e32 v177, 0xee00, v160
	v_ashrrev_i32_e32 v139, 31, v138
	s_waitcnt lgkmcnt(0)
	v_mfma_f32_16x16x32_bf16 v[144:147], v[148:151], v[80:83], v[144:147]
	ds_read2_b64 v[148:151], v156 offset0:16 offset1:20
	v_lshlrev_b32_e32 v122, 1, v120
	s_add_i32 s26, s26, 64
	s_waitcnt lgkmcnt(0)
	v_mfma_f32_16x16x32_bf16 v[112:115], v[148:151], v[76:79], v[112:115]
	ds_read2_b64 v[148:151], v163 offset0:48 offset1:52
	s_cmpk_eq_i32 s26, 0xc0
	s_waitcnt lgkmcnt(0)
	v_mfma_f32_16x16x32_bf16 v[116:119], v[148:151], v[76:79], v[116:119]
	ds_read2_b64 v[148:151], v164 offset0:80 offset1:84
	s_waitcnt lgkmcnt(0)
	v_mfma_f32_16x16x32_bf16 v[140:143], v[148:151], v[76:79], v[140:143]
	ds_read2_b64 v[148:151], v165 offset0:112 offset1:116
	s_waitcnt lgkmcnt(0)
	v_mfma_f32_16x16x32_bf16 v[144:147], v[148:151], v[76:79], v[144:147]
	ds_read2_b64 v[148:151], v156 offset0:24 offset1:28
	s_waitcnt lgkmcnt(0)
	v_mfma_f32_16x16x32_bf16 v[112:115], v[148:151], v[72:75], v[112:115]
	ds_read2_b64 v[148:151], v163 offset0:56 offset1:60
	s_waitcnt lgkmcnt(0)
	v_mfma_f32_16x16x32_bf16 v[116:119], v[148:151], v[72:75], v[116:119]
	ds_read2_b64 v[148:151], v164 offset0:88 offset1:92
	s_waitcnt lgkmcnt(0)
	v_mfma_f32_16x16x32_bf16 v[140:143], v[148:151], v[72:75], v[140:143]
	ds_read2_b64 v[148:151], v165 offset0:120 offset1:124
	s_waitcnt lgkmcnt(0)
	v_mfma_f32_16x16x32_bf16 v[144:147], v[148:151], v[72:75], v[144:147]
	ds_read2_b64 v[148:151], v166 offset0:128 offset1:132
	s_waitcnt lgkmcnt(0)
	v_mfma_f32_16x16x32_bf16 v[112:115], v[148:151], v[68:71], v[112:115]
	ds_read2_b64 v[148:151], v167 offset0:160 offset1:164
	s_waitcnt lgkmcnt(0)
	v_mfma_f32_16x16x32_bf16 v[116:119], v[148:151], v[68:71], v[116:119]
	ds_read2_b64 v[148:151], v168 offset0:192 offset1:196
	s_waitcnt lgkmcnt(0)
	v_mfma_f32_16x16x32_bf16 v[140:143], v[148:151], v[68:71], v[140:143]
	ds_read2_b64 v[148:151], v169 offset0:224 offset1:228
	s_waitcnt lgkmcnt(0)
	v_mfma_f32_16x16x32_bf16 v[144:147], v[148:151], v[68:71], v[144:147]
	ds_read2_b64 v[148:151], v166 offset0:136 offset1:140
	s_waitcnt lgkmcnt(0)
	v_mfma_f32_16x16x32_bf16 v[112:115], v[148:151], v[48:51], v[112:115]
	ds_read2_b64 v[148:151], v167 offset0:168 offset1:172
	s_waitcnt lgkmcnt(0)
	v_mfma_f32_16x16x32_bf16 v[116:119], v[148:151], v[48:51], v[116:119]
	ds_read2_b64 v[148:151], v168 offset0:200 offset1:204
	s_waitcnt lgkmcnt(0)
	v_mfma_f32_16x16x32_bf16 v[140:143], v[148:151], v[48:51], v[140:143]
	ds_read2_b64 v[148:151], v169 offset0:232 offset1:236
	s_waitcnt lgkmcnt(0)
	v_mfma_f32_16x16x32_bf16 v[144:147], v[148:151], v[48:51], v[144:147]
	ds_read2_b64 v[148:151], v166 offset0:144 offset1:148
	s_waitcnt lgkmcnt(0)
	v_mfma_f32_16x16x32_bf16 v[112:115], v[148:151], v[44:47], v[112:115]
	ds_read2_b64 v[148:151], v167 offset0:176 offset1:180
	s_waitcnt lgkmcnt(0)
	v_mfma_f32_16x16x32_bf16 v[116:119], v[148:151], v[44:47], v[116:119]
	ds_read2_b64 v[148:151], v168 offset0:208 offset1:212
	s_waitcnt lgkmcnt(0)
	v_mfma_f32_16x16x32_bf16 v[140:143], v[148:151], v[44:47], v[140:143]
	ds_read2_b64 v[148:151], v169 offset0:240 offset1:244
	s_waitcnt lgkmcnt(0)
	v_mfma_f32_16x16x32_bf16 v[144:147], v[148:151], v[44:47], v[144:147]
	ds_read2_b64 v[148:151], v166 offset0:152 offset1:156
	s_waitcnt lgkmcnt(0)
	v_mfma_f32_16x16x32_bf16 v[112:115], v[148:151], v[28:31], v[112:115]
	ds_read2_b64 v[148:151], v167 offset0:184 offset1:188
	s_waitcnt lgkmcnt(0)
	v_mfma_f32_16x16x32_bf16 v[116:119], v[148:151], v[28:31], v[116:119]
	ds_read2_b64 v[148:151], v168 offset0:216 offset1:220
	s_waitcnt lgkmcnt(0)
	v_mfma_f32_16x16x32_bf16 v[140:143], v[148:151], v[28:31], v[140:143]
	ds_read2_b64 v[148:151], v169 offset0:248 offset1:252
	s_nop 0
	ds_write2_b32 v170, v112, v113 offset1:132
	ds_write2_b32 v171, v114, v115 offset0:8 offset1:140
	s_waitcnt lgkmcnt(2)
	v_mfma_f32_16x16x32_bf16 v[144:147], v[148:151], v[28:31], v[144:147]
	ds_write2_b32 v172, v116, v117 offset0:64 offset1:196
	ds_write2_b32 v173, v118, v119 offset0:72 offset1:204
	ds_write2_b32 v174, v140, v141 offset1:132
	ds_write2_b32 v175, v142, v143 offset0:8 offset1:140
	s_nop 3
	ds_write2_b32 v176, v144, v145 offset0:64 offset1:196
	ds_write2_b32 v177, v146, v147 offset0:72 offset1:204
	s_waitcnt lgkmcnt(0)
	s_barrier
	ds_read_b128 v[112:115], v161 offset:34816
	ds_read_b128 v[116:119], v161 offset:34832
	ds_read_b128 v[178:181], v161 offset:34848
	ds_read_b128 v[146:149], v161 offset:34864
	v_lshlrev_b32_e32 v140, 16, v103
	v_and_b32_e32 v141, 0xffff0000, v103
	v_lshlrev_b32_e32 v142, 16, v111
	v_and_b32_e32 v143, 0xffff0000, v111
	v_pk_add_f32 v[140:141], v[142:143], v[140:141]
	v_and_b32_e32 v103, 0xffff0000, v110
	s_waitcnt lgkmcnt(0)
	v_pk_add_f32 v[140:141], v[140:141], v[148:149]
	v_lshlrev_b32_e32 v148, 16, v102
	v_and_b32_e32 v149, 0xffff0000, v102
	v_lshlrev_b32_e32 v102, 16, v110
	v_pk_add_f32 v[102:103], v[102:103], v[148:149]
	v_lshlrev_b32_e32 v142, 16, v107
	v_pk_add_f32 v[102:103], v[102:103], v[146:147]
	v_lshlrev_b32_e32 v146, 16, v106
	v_and_b32_e32 v147, 0xffff0000, v106
	v_and_b32_e32 v143, 0xffff0000, v107
	v_mul_f32_e32 v106, 0xbfb8aa3b, v146
	v_mul_f32_e32 v107, 0xbfb8aa3b, v147
	v_exp_f32_e32 v106, v106
	v_exp_f32_e32 v107, v107
	v_lshlrev_b32_e32 v148, 16, v109
	v_and_b32_e32 v149, 0xffff0000, v109
	v_add_f32_e32 v106, 1.0, v106
	v_add_f32_e32 v107, 1.0, v107
	v_rcp_f32_e32 v106, v106
	v_rcp_f32_e32 v107, v107
	v_pk_mul_f32 v[110:111], v[102:103], v[102:103]
	v_pk_mul_f32 v[144:145], v[140:141], v[140:141]
	v_pk_mul_f32 v[106:107], v[106:107], v[146:147]
	v_lshlrev_b32_e32 v146, 16, v101
	v_and_b32_e32 v147, 0xffff0000, v101
	v_pk_add_f32 v[146:147], v[148:149], v[146:147]
	v_lshlrev_b32_e32 v148, 16, v105
	v_mul_f32_e32 v101, 0xbfb8aa3b, v148
	v_exp_f32_e32 v101, v101
	v_and_b32_e32 v149, 0xffff0000, v105
	v_pk_add_f32 v[146:147], v[146:147], v[180:181]
	v_add_f32_e32 v101, 1.0, v101
	v_rcp_f32_e32 v180, v101
	v_mul_f32_e32 v101, 0xbfb8aa3b, v149
	v_exp_f32_e32 v101, v101
	v_pk_mul_f32 v[150:151], v[146:147], v[146:147]
	v_add_f32_e32 v101, 1.0, v101
	v_rcp_f32_e32 v181, v101
	v_and_b32_e32 v101, 0xffff0000, v108
	v_pk_mul_f32 v[148:149], v[180:181], v[148:149]
	v_lshlrev_b32_e32 v180, 16, v100
	v_and_b32_e32 v181, 0xffff0000, v100
	v_lshlrev_b32_e32 v100, 16, v108
	v_pk_add_f32 v[100:101], v[100:101], v[180:181]
	v_lshlrev_b32_e32 v180, 16, v99
	v_pk_add_f32 v[100:101], v[100:101], v[178:179]
	v_lshlrev_b32_e32 v178, 16, v104
	v_and_b32_e32 v179, 0xffff0000, v104
	v_mul_f32_e32 v104, 0xbfb8aa3b, v178
	v_mul_f32_e32 v105, 0xbfb8aa3b, v179
	v_exp_f32_e32 v104, v104
	v_exp_f32_e32 v105, v105
	v_and_b32_e32 v181, 0xffff0000, v99
	v_and_b32_e32 v99, 0xffff0000, v94
	v_add_f32_e32 v104, 1.0, v104
	v_add_f32_e32 v105, 1.0, v105
	v_rcp_f32_e32 v104, v104
	v_rcp_f32_e32 v105, v105
	v_pk_mul_f32 v[108:109], v[100:101], v[100:101]
	v_pk_mul_f32 v[104:105], v[104:105], v[178:179]
	v_lshlrev_b32_e32 v178, 16, v91
	v_and_b32_e32 v179, 0xffff0000, v91
	v_pk_add_f32 v[178:179], v[180:181], v[178:179]
	s_nop 0
	v_pk_add_f32 v[118:119], v[178:179], v[118:119]
	v_lshlrev_b32_e32 v178, 16, v95
	v_mul_f32_e32 v91, 0xbfb8aa3b, v178
	v_exp_f32_e32 v91, v91
	v_and_b32_e32 v179, 0xffff0000, v95
	v_pk_mul_f32 v[180:181], v[118:119], v[118:119]
	v_add_f32_e32 v91, 1.0, v91
	v_rcp_f32_e32 v182, v91
	v_mul_f32_e32 v91, 0xbfb8aa3b, v179
	v_exp_f32_e32 v91, v91
	s_nop 0
	v_add_f32_e32 v91, 1.0, v91
	v_rcp_f32_e32 v183, v91
	v_and_b32_e32 v91, 0xffff0000, v98
	v_pk_mul_f32 v[178:179], v[182:183], v[178:179]
	v_lshlrev_b32_e32 v182, 16, v90
	v_and_b32_e32 v183, 0xffff0000, v90
	v_lshlrev_b32_e32 v90, 16, v98
	v_pk_add_f32 v[90:91], v[90:91], v[182:183]
	v_lshlrev_b32_e32 v98, 16, v94
	v_pk_add_f32 v[90:91], v[90:91], v[116:117]
	v_mul_f32_e32 v116, 0xbfb8aa3b, v98
	v_mul_f32_e32 v117, 0xbfb8aa3b, v99
	v_exp_f32_e32 v116, v116
	v_exp_f32_e32 v117, v117
	v_lshlrev_b32_e32 v182, 16, v97
	v_and_b32_e32 v183, 0xffff0000, v97
	v_add_f32_e32 v116, 1.0, v116
	v_add_f32_e32 v117, 1.0, v117
	v_rcp_f32_e32 v116, v116
	v_rcp_f32_e32 v117, v117
	v_and_b32_e32 v97, 0xffff0000, v92
	v_pk_mul_f32 v[94:95], v[90:91], v[90:91]
	v_pk_mul_f32 v[98:99], v[116:117], v[98:99]
	v_lshlrev_b32_e32 v116, 16, v89
	v_and_b32_e32 v117, 0xffff0000, v89
	v_pk_add_f32 v[116:117], v[182:183], v[116:117]
	s_nop 0
	v_pk_add_f32 v[114:115], v[116:117], v[114:115]
	v_lshlrev_b32_e32 v116, 16, v93
	v_mul_f32_e32 v89, 0xbfb8aa3b, v116
	v_exp_f32_e32 v89, v89
	v_and_b32_e32 v117, 0xffff0000, v93
	v_pk_mul_f32 v[182:183], v[114:115], v[114:115]
	v_add_f32_e32 v89, 1.0, v89
	v_rcp_f32_e32 v184, v89
	v_mul_f32_e32 v89, 0xbfb8aa3b, v117
	v_exp_f32_e32 v89, v89
	s_nop 0
	v_add_f32_e32 v89, 1.0, v89
	v_rcp_f32_e32 v185, v89
	v_and_b32_e32 v89, 0xffff0000, v96
	v_pk_mul_f32 v[116:117], v[184:185], v[116:117]
	v_lshlrev_b32_e32 v184, 16, v88
	v_and_b32_e32 v185, 0xffff0000, v88
	v_lshlrev_b32_e32 v88, 16, v96
	v_pk_add_f32 v[88:89], v[88:89], v[184:185]
	v_lshlrev_b32_e32 v96, 16, v92
	v_pk_add_f32 v[88:89], v[88:89], v[112:113]
	v_mul_f32_e32 v112, 0xbfb8aa3b, v96
	v_pk_mul_f32 v[92:93], v[88:89], v[88:89]
	v_mul_f32_e32 v113, 0xbfb8aa3b, v97
	v_add_f32_e32 v92, v92, v93
	v_add_f32_e32 v92, v182, v92
	v_add_f32_e32 v92, v183, v92
	v_add_f32_e32 v92, v94, v92
	v_add_f32_e32 v92, v95, v92
	v_add_f32_e32 v92, v180, v92
	v_add_f32_e32 v92, v181, v92
	v_add_f32_e32 v92, v108, v92
	v_add_f32_e32 v92, v109, v92
	v_add_f32_e32 v92, v150, v92
	v_add_f32_e32 v92, v151, v92
	v_add_f32_e32 v92, v110, v92
	v_add_f32_e32 v92, v111, v92
	v_add_f32_e32 v92, v144, v92
	v_add_f32_e32 v92, v145, v92
	ds_bpermute_b32 v93, v153, v92
	v_exp_f32_e32 v112, v112
	v_exp_f32_e32 v113, v113
	s_waitcnt vmcnt(3)
	v_mov_b64_e32 v[110:111], v[34:35]
	v_mov_b64_e32 v[108:109], v[32:33]
	s_waitcnt lgkmcnt(0)
	v_add_f32_e32 v92, v92, v93
	ds_bpermute_b32 v93, v154, v92
	v_add_f32_e32 v112, 1.0, v112
	v_add_f32_e32 v113, 1.0, v113
	v_rcp_f32_e32 v112, v112
	v_rcp_f32_e32 v113, v113
	s_waitcnt lgkmcnt(0)
	v_add_f32_e32 v92, v92, v93
	ds_bpermute_b32 v93, v155, v92
	v_pk_mul_f32 v[96:97], v[112:113], v[96:97]
	s_waitcnt lgkmcnt(0)
	v_add_f32_e32 v92, v92, v93
	v_fmamk_f32 v92, v92, 0x3c000000, v158
	v_cmp_gt_f32_e32 vcc, s21, v92
	v_mul_f32_e32 v93, 0x4b800000, v92
	s_nop 0
	v_cndmask_b32_e32 v92, v92, v93, vcc
	v_rsq_f32_e32 v92, v92
	s_nop 0
	v_mul_f32_e32 v93, 0x45800000, v92
	v_cndmask_b32_e32 v92, v92, v93, vcc
	v_pk_mul_f32 v[90:91], v[90:91], v[92:93] op_sel_hi:[1,0]
	v_pk_mul_f32 v[88:89], v[88:89], v[92:93] op_sel_hi:[1,0]
	v_pk_mul_f32 v[90:91], v[8:9], v[90:91]
	v_pk_mul_f32 v[88:89], v[12:13], v[88:89]
	v_pk_mul_f32 v[90:91], v[98:99], v[90:91]
	v_pk_mul_f32 v[98:99], v[100:101], v[92:93] op_sel_hi:[1,0]
	v_pk_mul_f32 v[88:89], v[96:97], v[88:89]
	v_pk_mul_f32 v[98:99], v[4:5], v[98:99]
	v_pk_mul_f32 v[94:95], v[114:115], v[92:93] op_sel_hi:[1,0]
	v_pk_mul_f32 v[96:97], v[118:119], v[92:93] op_sel_hi:[1,0]
	v_pk_mul_f32 v[98:99], v[104:105], v[98:99]
	v_pk_mul_f32 v[100:101], v[146:147], v[92:93] op_sel_hi:[1,0]
	v_pk_mul_f32 v[102:103], v[102:103], v[92:93] op_sel_hi:[1,0]
	v_mul_f32_e32 v93, 0xbfb8aa3b, v142
	v_mul_f32_e32 v105, 0xbfb8aa3b, v143
	v_exp_f32_e32 v93, v93
	v_exp_f32_e32 v105, v105
	v_pk_mul_f32 v[96:97], v[10:11], v[96:97]
	v_cvt_pk_bf16_f32 v90, v90, v91
	v_add_f32_e32 v93, 1.0, v93
	v_add_f32_e32 v105, 1.0, v105
	v_pk_mul_f32 v[96:97], v[178:179], v[96:97]
	v_rcp_f32_e32 v104, v93
	v_rcp_f32_e32 v105, v105
	v_cvt_pk_bf16_f32 v91, v96, v97
	v_lshlrev_b64 v[96:97], 11, v[138:139]
	v_lshl_add_u64 v[96:97], s[0:1], 0, v[96:97]
	v_pk_mul_f32 v[92:93], v[140:141], v[92:93] op_sel_hi:[1,0]
	v_lshl_add_u64 v[96:97], v[96:97], 0, s[12:13]
	v_pk_mul_f32 v[94:95], v[14:15], v[94:95]
	v_pk_mul_f32 v[100:101], v[6:7], v[100:101]
	v_pk_mul_f32 v[102:103], v[0:1], v[102:103]
	v_pk_mul_f32 v[92:93], v[2:3], v[92:93]
	v_pk_mul_f32 v[104:105], v[104:105], v[142:143]
	v_lshl_add_u64 v[96:97], v[96:97], 0, v[122:123]
	v_pk_mul_f32 v[94:95], v[116:117], v[94:95]
	v_pk_mul_f32 v[100:101], v[148:149], v[100:101]
	v_pk_mul_f32 v[102:103], v[106:107], v[102:103]
	v_pk_mul_f32 v[104:105], v[104:105], v[92:93]
	v_cvt_pk_bf16_f32 v92, v98, v99
	v_lshl_add_u64 v[98:99], v[96:97], 0, s[16:17]
	v_add_co_u32_e32 v96, vcc, 0x1971b000, v96
	v_cvt_pk_bf16_f32 v88, v88, v89
	v_cvt_pk_bf16_f32 v89, v94, v95
	v_cvt_pk_bf16_f32 v93, v100, v101
	v_cvt_pk_bf16_f32 v94, v102, v103
	v_cvt_pk_bf16_f32 v95, v104, v105
	v_addc_co_u32_e32 v97, vcc, 0, v97, vcc
	global_store_dwordx4 v[96:97], v[88:91], off offset:1024
	global_store_dwordx4 v[98:99], v[92:95], off offset:16
	s_waitcnt vmcnt(3)
	v_mov_b64_e32 v[106:107], v[38:39]
	v_mov_b64_e32 v[98:99], v[22:23]
	s_waitcnt vmcnt(2)
	v_mov_b64_e32 v[94:95], v[18:19]
	v_mov_b64_e32 v[102:103], v[42:43]
	v_mov_b64_e32 v[90:91], v[26:27]
	v_mov_b64_e32 v[104:105], v[36:37]
	v_mov_b64_e32 v[92:93], v[16:17]
	v_mov_b64_e32 v[96:97], v[20:21]
	v_mov_b64_e32 v[100:101], v[40:41]
	v_mov_b64_e32 v[88:89], v[24:25]
	s_cbranch_scc0 .LBB0_497
	ds_write_b128 v159, v[52:55]
	ds_write_b128 v159, v[64:67] offset:8704
	ds_write_b128 v159, v[56:59] offset:17408
	ds_write_b128 v159, v[60:63] offset:26112
	s_waitcnt lgkmcnt(0)
	s_barrier
	ds_read2_b64 v[52:55], v156 offset1:4
	ds_read2_b64 v[56:59], v163 offset0:32 offset1:36
	ds_read2_b64 v[60:63], v164 offset0:64 offset1:68
	ds_read2_b64 v[64:67], v165 offset0:96 offset1:100
	s_waitcnt lgkmcnt(3)
	v_mfma_f32_16x16x32_bf16 v[52:55], v[52:55], v[84:87], 0
	ds_read2_b64 v[88:91], v156 offset0:8 offset1:12
	v_readlane_b32 s28, v235, 0
	v_readlane_b32 s30, v235, 2
	s_waitcnt lgkmcnt(3)
	v_mfma_f32_16x16x32_bf16 v[56:59], v[56:59], v[84:87], 0
	s_add_i32 s23, s23, s30
	s_add_i32 s18, s18, s19
	s_cmpk_gt_i32 s23, 0xff
	s_waitcnt lgkmcnt(2)
	v_mfma_f32_16x16x32_bf16 v[60:63], v[60:63], v[84:87], 0
	v_readlane_b32 s29, v235, 1
	v_readlane_b32 s31, v235, 3
	s_waitcnt lgkmcnt(1)
	v_mfma_f32_16x16x32_bf16 v[64:67], v[64:67], v[84:87], 0
	ds_read2_b64 v[84:87], v163 offset0:40 offset1:44
	s_waitcnt lgkmcnt(1)
	v_mfma_f32_16x16x32_bf16 v[52:55], v[88:91], v[80:83], v[52:55]
	ds_read2_b64 v[88:91], v164 offset0:72 offset1:76
	s_waitcnt lgkmcnt(1)
	v_mfma_f32_16x16x32_bf16 v[56:59], v[84:87], v[80:83], v[56:59]
	ds_read2_b64 v[84:87], v165 offset0:104 offset1:108
	s_waitcnt lgkmcnt(1)
	v_mfma_f32_16x16x32_bf16 v[60:63], v[88:91], v[80:83], v[60:63]
	ds_read2_b64 v[88:91], v156 offset0:16 offset1:20
	s_waitcnt lgkmcnt(1)
	v_mfma_f32_16x16x32_bf16 v[64:67], v[84:87], v[80:83], v[64:67]
	ds_read2_b64 v[80:83], v163 offset0:48 offset1:52
	ds_read2_b64 v[84:87], v164 offset0:80 offset1:84
	s_waitcnt lgkmcnt(1)
	v_mfma_f32_16x16x32_bf16 v[56:59], v[80:83], v[76:79], v[56:59]
	ds_read2_b64 v[80:83], v165 offset0:112 offset1:116
	v_mfma_f32_16x16x32_bf16 v[52:55], v[88:91], v[76:79], v[52:55]
	s_waitcnt lgkmcnt(1)
	v_mfma_f32_16x16x32_bf16 v[60:63], v[84:87], v[76:79], v[60:63]
	ds_read2_b64 v[84:87], v156 offset0:24 offset1:28
	s_waitcnt lgkmcnt(1)
	v_mfma_f32_16x16x32_bf16 v[64:67], v[80:83], v[76:79], v[64:67]
	ds_read2_b64 v[76:79], v163 offset0:56 offset1:60
	ds_read2_b64 v[80:83], v164 offset0:88 offset1:92
	s_waitcnt lgkmcnt(1)
	v_mfma_f32_16x16x32_bf16 v[56:59], v[76:79], v[72:75], v[56:59]
	ds_read2_b64 v[76:79], v165 offset0:120 offset1:124
	v_mfma_f32_16x16x32_bf16 v[52:55], v[84:87], v[72:75], v[52:55]
	s_waitcnt lgkmcnt(1)
	v_mfma_f32_16x16x32_bf16 v[60:63], v[80:83], v[72:75], v[60:63]
	ds_read2_b64 v[80:83], v166 offset0:128 offset1:132
	s_waitcnt lgkmcnt(1)
	v_mfma_f32_16x16x32_bf16 v[64:67], v[76:79], v[72:75], v[64:67]
	ds_read2_b64 v[72:75], v167 offset0:160 offset1:164
	ds_read2_b64 v[76:79], v168 offset0:192 offset1:196
	s_waitcnt lgkmcnt(1)
	v_mfma_f32_16x16x32_bf16 v[56:59], v[72:75], v[68:71], v[56:59]
	ds_read2_b64 v[72:75], v169 offset0:224 offset1:228
	v_mfma_f32_16x16x32_bf16 v[52:55], v[80:83], v[68:71], v[52:55]
	s_waitcnt lgkmcnt(1)
	v_mfma_f32_16x16x32_bf16 v[60:63], v[76:79], v[68:71], v[60:63]
	ds_read2_b64 v[76:79], v166 offset0:136 offset1:140
	s_waitcnt lgkmcnt(1)
	v_mfma_f32_16x16x32_bf16 v[64:67], v[72:75], v[68:71], v[64:67]
	ds_read2_b64 v[68:71], v167 offset0:168 offset1:172
	ds_read2_b64 v[72:75], v168 offset0:200 offset1:204
	s_waitcnt lgkmcnt(1)
	v_mfma_f32_16x16x32_bf16 v[56:59], v[68:71], v[48:51], v[56:59]
	ds_read2_b64 v[68:71], v169 offset0:232 offset1:236
	v_mfma_f32_16x16x32_bf16 v[52:55], v[76:79], v[48:51], v[52:55]
	s_waitcnt lgkmcnt(1)
	v_mfma_f32_16x16x32_bf16 v[60:63], v[72:75], v[48:51], v[60:63]
	ds_read2_b64 v[72:75], v166 offset0:144 offset1:148
	s_waitcnt lgkmcnt(1)
	v_mfma_f32_16x16x32_bf16 v[48:51], v[68:71], v[48:51], v[64:67]
	ds_read2_b64 v[68:71], v168 offset0:208 offset1:212
	s_nop 1
	ds_read2_b64 v[64:67], v167 offset0:176 offset1:180
	s_waitcnt lgkmcnt(0)
	v_mfma_f32_16x16x32_bf16 v[56:59], v[64:67], v[44:47], v[56:59]
	ds_read2_b64 v[64:67], v169 offset0:240 offset1:244
	v_mfma_f32_16x16x32_bf16 v[60:63], v[68:71], v[44:47], v[60:63]
	ds_read2_b64 v[68:71], v166 offset0:152 offset1:156
	v_mfma_f32_16x16x32_bf16 v[52:55], v[72:75], v[44:47], v[52:55]
	s_waitcnt lgkmcnt(1)
	v_mfma_f32_16x16x32_bf16 v[44:47], v[64:67], v[44:47], v[48:51]
	s_nop 2
	ds_read2_b64 v[48:51], v167 offset0:184 offset1:188
	s_waitcnt lgkmcnt(1)
	v_mfma_f32_16x16x32_bf16 v[52:55], v[68:71], v[28:31], v[52:55]
	ds_read2_b64 v[64:67], v168 offset0:216 offset1:220
	ds_read2_b64 v[68:71], v169 offset0:248 offset1:252
	s_waitcnt lgkmcnt(2)
	v_mfma_f32_16x16x32_bf16 v[48:51], v[48:51], v[28:31], v[56:59]
	s_nop 3
	ds_write2_b32 v170, v52, v53 offset1:132
	ds_write2_b32 v171, v54, v55 offset0:8 offset1:140
	s_nop 1
	ds_write2_b32 v172, v48, v49 offset0:64 offset1:196
	s_waitcnt lgkmcnt(4)
	v_mfma_f32_16x16x32_bf16 v[52:55], v[64:67], v[28:31], v[60:63]
	ds_write2_b32 v173, v50, v51 offset0:72 offset1:204
	s_nop 6
	ds_write2_b32 v174, v52, v53 offset1:132
	ds_write2_b32 v175, v54, v55 offset0:8 offset1:140
	s_waitcnt lgkmcnt(6)
	v_mfma_f32_16x16x32_bf16 v[28:31], v[68:71], v[28:31], v[44:47]
	v_lshlrev_b32_e32 v62, 16, v38
	v_and_b32_e32 v63, 0xffff0000, v38
	s_nop 5
	ds_write2_b32 v176, v28, v29 offset0:64 offset1:196
	ds_write2_b32 v177, v30, v31 offset0:72 offset1:204
	v_lshlrev_b32_e32 v30, 16, v35
	v_and_b32_e32 v31, 0xffff0000, v35
	v_mul_f32_e32 v35, 0xbfb8aa3b, v62
	v_mul_f32_e32 v38, 0xbfb8aa3b, v63
	v_exp_f32_e32 v35, v35
	v_exp_f32_e32 v38, v38
	v_lshlrev_b32_e32 v28, 16, v43
	v_and_b32_e32 v29, 0xffff0000, v43
	v_lshlrev_b32_e32 v60, 16, v42
	v_and_b32_e32 v61, 0xffff0000, v42
	v_lshlrev_b32_e32 v42, 16, v34
	v_and_b32_e32 v43, 0xffff0000, v34
	v_add_f32_e32 v34, 1.0, v35
	v_add_f32_e32 v35, 1.0, v38
	s_waitcnt lgkmcnt(0)
	s_barrier
	ds_read_b128 v[44:47], v161 offset:34816
	ds_read_b128 v[48:51], v161 offset:34832
	ds_read_b128 v[52:55], v161 offset:34848
	ds_read_b128 v[56:59], v161 offset:34864
	v_rcp_f32_e32 v34, v34
	v_rcp_f32_e32 v35, v35
	v_pk_add_f32 v[28:29], v[28:29], v[30:31]
	v_lshlrev_b32_e32 v70, 16, v24
	s_waitcnt lgkmcnt(0)
	v_pk_add_f32 v[30:31], v[28:29], v[58:59]
	v_pk_mul_f32 v[34:35], v[34:35], v[62:63]
	v_lshlrev_b32_e32 v62, 16, v37
	v_lshlrev_b32_e32 v28, 16, v39
	v_and_b32_e32 v29, 0xffff0000, v39
	v_pk_add_f32 v[38:39], v[60:61], v[42:43]
	v_and_b32_e32 v63, 0xffff0000, v37
	v_mul_f32_e32 v37, 0xbfb8aa3b, v62
	v_pk_add_f32 v[38:39], v[38:39], v[56:57]
	v_lshlrev_b32_e32 v56, 16, v41
	v_and_b32_e32 v57, 0xffff0000, v41
	v_exp_f32_e32 v37, v37
	v_mul_f32_e32 v41, 0xbfb8aa3b, v63
	v_exp_f32_e32 v41, v41
	v_lshlrev_b32_e32 v60, 16, v33
	v_and_b32_e32 v61, 0xffff0000, v33
	v_add_f32_e32 v33, 1.0, v37
	v_rcp_f32_e32 v64, v33
	v_add_f32_e32 v33, 1.0, v41
	v_rcp_f32_e32 v65, v33
	v_pk_add_f32 v[56:57], v[56:57], v[60:61]
	v_and_b32_e32 v41, 0xffff0000, v32
	v_and_b32_e32 v71, 0xffff0000, v24
	v_pk_mul_f32 v[60:61], v[64:65], v[62:63]
	v_lshlrev_b32_e32 v64, 16, v36
	v_and_b32_e32 v65, 0xffff0000, v36
	v_mul_f32_e32 v33, 0xbfb8aa3b, v64
	v_mul_f32_e32 v36, 0xbfb8aa3b, v65
	v_exp_f32_e32 v33, v33
	v_exp_f32_e32 v36, v36
	v_lshlrev_b32_e32 v62, 16, v40
	v_and_b32_e32 v63, 0xffff0000, v40
	v_lshlrev_b32_e32 v40, 16, v32
	v_add_f32_e32 v32, 1.0, v33
	v_add_f32_e32 v33, 1.0, v36
	v_rcp_f32_e32 v32, v32
	v_rcp_f32_e32 v33, v33
	v_pk_add_f32 v[36:37], v[62:63], v[40:41]
	v_lshlrev_b32_e32 v62, 16, v23
	v_pk_add_f32 v[36:37], v[36:37], v[52:53]
	v_pk_mul_f32 v[32:33], v[32:33], v[64:65]
	v_lshlrev_b32_e32 v64, 16, v19
	v_and_b32_e32 v65, 0xffff0000, v19
	v_mul_f32_e32 v19, 0xbfb8aa3b, v64
	v_lshlrev_b32_e32 v52, 16, v27
	v_and_b32_e32 v53, 0xffff0000, v27
	v_exp_f32_e32 v19, v19
	v_mul_f32_e32 v27, 0xbfb8aa3b, v65
	v_exp_f32_e32 v27, v27
	v_and_b32_e32 v63, 0xffff0000, v23
	v_add_f32_e32 v19, 1.0, v19
	v_rcp_f32_e32 v66, v19
	v_add_f32_e32 v19, 1.0, v27
	v_rcp_f32_e32 v67, v19
	v_pk_add_f32 v[52:53], v[52:53], v[62:63]
	v_and_b32_e32 v27, 0xffff0000, v22
	v_lshlrev_b32_e32 v24, 16, v20
	v_pk_mul_f32 v[62:63], v[66:67], v[64:65]
	v_lshlrev_b32_e32 v64, 16, v26
	v_and_b32_e32 v65, 0xffff0000, v26
	v_lshlrev_b32_e32 v26, 16, v22
	v_pk_add_f32 v[22:23], v[64:65], v[26:27]
	v_lshlrev_b32_e32 v64, 16, v25
	v_and_b32_e32 v65, 0xffff0000, v25
	v_lshlrev_b32_e32 v66, 16, v21
	v_and_b32_e32 v67, 0xffff0000, v21
	v_pk_add_f32 v[64:65], v[64:65], v[66:67]
	v_lshlrev_b32_e32 v66, 16, v17
	v_mul_f32_e32 v21, 0xbfb8aa3b, v66
	v_exp_f32_e32 v21, v21
	v_and_b32_e32 v25, 0xffff0000, v20
	v_and_b32_e32 v67, 0xffff0000, v17
	v_lshlrev_b32_e32 v26, 16, v18
	v_add_f32_e32 v17, 1.0, v21
	v_pk_add_f32 v[20:21], v[70:71], v[24:25]
	v_pk_add_f32 v[46:47], v[64:65], v[46:47]
	v_pk_add_f32 v[20:21], v[20:21], v[44:45]
	v_and_b32_e32 v27, 0xffff0000, v18
	v_pk_mul_f32 v[24:25], v[20:21], v[20:21]
	v_mul_f32_e32 v18, 0xbfb8aa3b, v26
	v_pk_mul_f32 v[64:65], v[46:47], v[46:47]
	v_add_f32_e32 v24, v24, v25
	v_pk_add_f32 v[22:23], v[22:23], v[48:49]
	v_exp_f32_e32 v48, v18
	v_mul_f32_e32 v18, 0xbfb8aa3b, v27
	v_add_f32_e32 v24, v64, v24
	v_exp_f32_e32 v49, v18
	v_pk_mul_f32 v[18:19], v[22:23], v[22:23]
	v_add_f32_e32 v24, v65, v24
	v_pk_add_f32 v[50:51], v[52:53], v[50:51]
	v_add_f32_e32 v18, v18, v24
	v_pk_mul_f32 v[52:53], v[50:51], v[50:51]
	v_add_f32_e32 v18, v19, v18
	v_add_f32_e32 v18, v52, v18
	v_pk_mul_f32 v[40:41], v[36:37], v[36:37]
	v_add_f32_e32 v18, v53, v18
	v_pk_add_f32 v[54:55], v[56:57], v[54:55]
	v_add_f32_e32 v18, v40, v18
	v_pk_mul_f32 v[56:57], v[54:55], v[54:55]
	v_add_f32_e32 v18, v41, v18
	v_add_f32_e32 v18, v56, v18
	v_pk_mul_f32 v[42:43], v[38:39], v[38:39]
	v_add_f32_e32 v18, v57, v18
	v_add_f32_e32 v18, v42, v18
	v_pk_mul_f32 v[58:59], v[30:31], v[30:31]
	v_add_f32_e32 v18, v43, v18
	v_add_f32_e32 v18, v58, v18
	v_add_f32_e32 v24, v59, v18
	v_rcp_f32_e32 v68, v17
	v_mul_f32_e32 v17, 0xbfb8aa3b, v67
	ds_bpermute_b32 v25, v153, v24
	v_exp_f32_e32 v17, v17
	v_lshlrev_b32_e32 v18, 16, v16
	v_and_b32_e32 v19, 0xffff0000, v16
	v_add_f32_e32 v48, 1.0, v48
	v_add_f32_e32 v17, 1.0, v17
	s_waitcnt lgkmcnt(0)
	v_add_f32_e32 v16, v24, v25
	v_rcp_f32_e32 v69, v17
	ds_bpermute_b32 v17, v154, v16
	v_mul_f32_e32 v24, 0xbfb8aa3b, v18
	v_exp_f32_e32 v24, v24
	v_mul_f32_e32 v25, 0xbfb8aa3b, v19
	v_exp_f32_e32 v25, v25
	s_waitcnt lgkmcnt(0)
	v_add_f32_e32 v40, v16, v17
	ds_bpermute_b32 v41, v155, v40
	v_add_f32_e32 v16, 1.0, v24
	v_add_f32_e32 v17, 1.0, v25
	v_rcp_f32_e32 v16, v16
	v_rcp_f32_e32 v17, v17
	s_waitcnt lgkmcnt(0)
	v_add_f32_e32 v24, v40, v41
	v_fmamk_f32 v24, v24, 0x3c000000, v158
	v_mul_f32_e32 v25, 0x4b800000, v24
	v_cmp_gt_f32_e32 vcc, s21, v24
	v_pk_mul_f32 v[16:17], v[16:17], v[18:19]
	v_add_f32_e32 v49, 1.0, v49
	v_cndmask_b32_e32 v24, v24, v25, vcc
	v_rsq_f32_e32 v40, v24
	v_rcp_f32_e32 v48, v48
	v_rcp_f32_e32 v49, v49
	v_mul_f32_e32 v18, 0x45800000, v40
	v_cndmask_b32_e32 v18, v40, v18, vcc
	v_pk_mul_f32 v[20:21], v[20:21], v[18:19] op_sel_hi:[1,0]
	v_pk_mul_f32 v[24:25], v[48:49], v[26:27]
	v_pk_mul_f32 v[12:13], v[12:13], v[20:21]
	v_mul_f32_e32 v20, 0xbfb8aa3b, v29
	v_pk_mul_f32 v[12:13], v[16:17], v[12:13]
	v_pk_mul_f32 v[16:17], v[46:47], v[18:19] op_sel_hi:[1,0]
	v_exp_f32_e32 v20, v20
	v_pk_mul_f32 v[14:15], v[14:15], v[16:17]
	v_pk_mul_f32 v[16:17], v[22:23], v[18:19] op_sel_hi:[1,0]
	v_pk_mul_f32 v[26:27], v[68:69], v[66:67]
	v_pk_mul_f32 v[8:9], v[8:9], v[16:17]
	v_pk_mul_f32 v[16:17], v[50:51], v[18:19] op_sel_hi:[1,0]
	v_pk_mul_f32 v[8:9], v[24:25], v[8:9]
	v_pk_mul_f32 v[10:11], v[10:11], v[16:17]
	v_pk_mul_f32 v[16:17], v[36:37], v[18:19] op_sel_hi:[1,0]
	v_pk_mul_f32 v[10:11], v[62:63], v[10:11]
	v_pk_mul_f32 v[4:5], v[4:5], v[16:17]
	v_pk_mul_f32 v[16:17], v[54:55], v[18:19] op_sel_hi:[1,0]
	v_pk_mul_f32 v[14:15], v[26:27], v[14:15]
	v_pk_mul_f32 v[6:7], v[6:7], v[16:17]
	v_pk_mul_f32 v[16:17], v[38:39], v[18:19] op_sel_hi:[1,0]
	v_mul_f32_e32 v19, 0xbfb8aa3b, v28
	v_exp_f32_e32 v19, v19
	v_pk_mul_f32 v[0:1], v[0:1], v[16:17]
	v_add_f32_e32 v17, 1.0, v20
	v_rcp_f32_e32 v17, v17
	v_add_f32_e32 v16, 1.0, v19
	v_rcp_f32_e32 v16, v16
	v_pk_mul_f32 v[20:21], v[34:35], v[0:1]
	v_pk_mul_f32 v[0:1], v[30:31], v[18:19] op_sel_hi:[1,0]
	v_pk_mul_f32 v[4:5], v[32:33], v[4:5]
	v_pk_mul_f32 v[0:1], v[2:3], v[0:1]
	v_pk_mul_f32 v[2:3], v[16:17], v[28:29]
	v_pk_mul_f32 v[6:7], v[60:61], v[6:7]
	v_pk_mul_f32 v[16:17], v[2:3], v[0:1]
	v_cvt_pk_bf16_f32 v2, v8, v9
	v_add_u32_e32 v8, 0xc0, v132
	v_ashrrev_i32_e32 v9, 31, v8
	v_lshlrev_b64 v[8:9], 11, v[8:9]
	v_lshl_add_u64 v[8:9], s[0:1], 0, v[8:9]
	v_lshl_add_u64 v[8:9], v[8:9], 0, s[12:13]
	v_lshl_add_u64 v[8:9], v[8:9], 0, v[122:123]
	v_cvt_pk_bf16_f32 v3, v10, v11
	v_lshl_add_u64 v[10:11], v[8:9], 0, s[16:17]
	v_add_co_u32_e32 v8, vcc, s22, v8
	v_cvt_pk_bf16_f32 v0, v12, v13
	v_cvt_pk_bf16_f32 v1, v14, v15
	v_addc_co_u32_e32 v9, vcc, 0, v9, vcc
	v_cvt_pk_bf16_f32 v4, v4, v5
	v_cvt_pk_bf16_f32 v5, v6, v7
	v_cvt_pk_bf16_f32 v6, v20, v21
	v_cvt_pk_bf16_f32 v7, v16, v17
	global_store_dwordx4 v[8:9], v[0:3], off offset:1024
	global_store_dwordx4 v[10:11], v[4:7], off offset:16
	s_barrier
	s_cbranch_scc0 .LBB0_496

.Lxb_poll_5:
	v_readfirstlane_b32 s98, v236
	v_mov_b32_e32 v237, 0x2c80
	v_mov_b32_e32 v239, 0

.LBB0_566:
	s_cmp_lg_u32 s60, 4
	s_cbranch_scc1 .Lp6kw_none
	v_readfirstlane_b32 s100, v186
	s_nop 0
	s_cmp_lg_u32 s100, 0
	s_cbranch_scc1 .Lp6kw_skip
	s_cmp_eq_u32 s98, 0
	s_cbranch_scc1 .Lp6kw_skip
	v_readlane_b32 s100, v235, 7
	v_readlane_b32 s101, v235, 8
	v_mov_b32_e32 v236, 0x3400
	v_mov_b32_e32 v239, 0
	s_nop 3

.Lp6kw_skip:
.Lp6kw_none:
	ds_read_b128 v[128:131], v165
	ds_read_b128 v[132:135], v165 offset:1024
	ds_read_b128 v[152:155], v165 offset:2048
	ds_read_b128 v[156:159], v165 offset:3072
	ds_read_b128 v[168:171], v166
	ds_read_b128 v[172:175], v166 offset:1024
	ds_read_b128 v[176:179], v166 offset:2048
	ds_read_b128 v[180:183], v166 offset:3072
	s_add_u32 s38, s36, 0x80
	s_addc_u32 s39, s37, 0
	s_cmp_eq_u32 s60, 12
	s_cselect_b32 s41, s21, s39
	s_cselect_b32 s40, s56, s38
	s_cselect_b32 s39, s23, s59
	s_cselect_b32 s38, s57, s58
	v_lshl_add_u64 v[160:161], s[36:37], 0, v[150:151]
	s_add_i32 m0, s46, 0xc000
	ds_read_b128 v[188:191], v167
	ds_read_b128 v[192:195], v167 offset:1024
	ds_read_b128 v[196:199], v167 offset:2048
	ds_read_b128 v[200:203], v167 offset:3072
	ds_read_b128 v[204:207], v167 offset:4096
	ds_read_b128 v[208:211], v167 offset:5120
	ds_read_b128 v[212:215], v167 offset:6144
	ds_read_b128 v[216:219], v167 offset:7168
	global_load_lds_dwordx4 v[160:161], off
	v_lshl_add_u64 v[160:161], s[36:37], 0, v[148:149]
	s_add_i32 m0, s46, 0xe000
	s_nop 0
	global_load_lds_dwordx4 v[160:161], off
	s_waitcnt vmcnt(8)
	s_waitcnt lgkmcnt(0)
	s_barrier
	s_setprio 1
	s_waitcnt lgkmcnt(0)
	v_mfma_f32_16x16x32_bf16 v[124:127], v[128:131], v[188:191], v[124:127]
	v_mfma_f32_16x16x32_bf16 v[120:123], v[152:155], v[188:191], v[120:123]
	v_mfma_f32_16x16x32_bf16 v[116:119], v[128:131], v[196:199], v[116:119]
	v_mfma_f32_16x16x32_bf16 v[112:115], v[152:155], v[196:199], v[112:115]
	v_mfma_f32_16x16x32_bf16 v[108:111], v[128:131], v[204:207], v[108:111]
	v_mfma_f32_16x16x32_bf16 v[104:107], v[152:155], v[204:207], v[104:107]
	v_mfma_f32_16x16x32_bf16 v[100:103], v[128:131], v[212:215], v[100:103]
	v_mfma_f32_16x16x32_bf16 v[96:99], v[152:155], v[212:215], v[96:99]
	v_mfma_f32_16x16x32_bf16 v[124:127], v[132:135], v[192:195], v[124:127]
	v_mfma_f32_16x16x32_bf16 v[120:123], v[156:159], v[192:195], v[120:123]
	v_mfma_f32_16x16x32_bf16 v[116:119], v[132:135], v[200:203], v[116:119]
	v_mfma_f32_16x16x32_bf16 v[112:115], v[156:159], v[200:203], v[112:115]
	v_mfma_f32_16x16x32_bf16 v[108:111], v[132:135], v[208:211], v[108:111]
	v_mfma_f32_16x16x32_bf16 v[104:107], v[156:159], v[208:211], v[104:107]
	v_mfma_f32_16x16x32_bf16 v[100:103], v[132:135], v[216:219], v[100:103]
	v_mfma_f32_16x16x32_bf16 v[96:99], v[156:159], v[216:219], v[96:99]
	s_setprio 0
	s_setprio 1
	v_mfma_f32_16x16x32_bf16 v[68:71], v[168:171], v[188:191], v[68:71]
	v_mfma_f32_16x16x32_bf16 v[64:67], v[176:179], v[188:191], v[64:67]
	v_mfma_f32_16x16x32_bf16 v[52:55], v[168:171], v[196:199], v[52:55]
	v_mfma_f32_16x16x32_bf16 v[48:51], v[176:179], v[196:199], v[48:51]
	v_mfma_f32_16x16x32_bf16 v[44:47], v[168:171], v[204:207], v[44:47]
	v_mfma_f32_16x16x32_bf16 v[40:43], v[176:179], v[204:207], v[40:43]
	v_mfma_f32_16x16x32_bf16 v[36:39], v[168:171], v[212:215], v[36:39]
	v_mfma_f32_16x16x32_bf16 v[32:35], v[176:179], v[212:215], v[32:35]
	v_mfma_f32_16x16x32_bf16 v[68:71], v[172:175], v[192:195], v[68:71]
	v_mfma_f32_16x16x32_bf16 v[64:67], v[180:183], v[192:195], v[64:67]
	v_mfma_f32_16x16x32_bf16 v[52:55], v[172:175], v[200:203], v[52:55]
	v_mfma_f32_16x16x32_bf16 v[48:51], v[180:183], v[200:203], v[48:51]
	v_mfma_f32_16x16x32_bf16 v[44:47], v[172:175], v[208:211], v[44:47]
	v_mfma_f32_16x16x32_bf16 v[40:43], v[180:183], v[208:211], v[40:43]
	v_mfma_f32_16x16x32_bf16 v[36:39], v[172:175], v[216:219], v[36:39]
	v_mfma_f32_16x16x32_bf16 v[32:35], v[180:183], v[216:219], v[32:35]
	s_setprio 0
	s_barrier
	s_add_i32 s61, s54, s45
	v_lshl_add_u64 v[160:161], s[38:39], 0, v[146:147]
	s_mov_b32 m0, s61
	ds_read_b128 v[188:191], v167 offset:16384
	ds_read_b128 v[192:195], v167 offset:17408
	ds_read_b128 v[196:199], v167 offset:18432
	ds_read_b128 v[200:203], v167 offset:19456
	ds_read_b128 v[204:207], v167 offset:20480
	ds_read_b128 v[208:211], v167 offset:21504
	ds_read_b128 v[212:215], v167 offset:22528
	ds_read_b128 v[216:219], v167 offset:23552
	global_load_lds_dwordx4 v[160:161], off
	s_add_i32 m0, s61, 0x2000
	s_add_u32 s62, s38, 0x40000
	v_lshl_add_u64 v[184:185], s[38:39], 0, v[140:141]
	s_addc_u32 s63, s39, 0
	s_add_i32 s61, s55, s45
	global_load_lds_dwordx4 v[184:185], off
	v_lshl_add_u64 v[220:221], s[62:63], 0, v[146:147]
	s_mov_b32 m0, s61
	v_lshl_add_u64 v[222:223], s[40:41], 0, v[136:137]
	global_load_lds_dwordx4 v[220:221], off
	v_lshl_add_u64 v[220:221], s[62:63], 0, v[140:141]
	s_add_i32 m0, s61, 0x2000
	s_nop 0
	global_load_lds_dwordx4 v[220:221], off
	v_lshl_add_u64 v[220:221], s[40:41], 0, v[142:143]
	s_mov_b32 m0, s46
	s_nop 0
	global_load_lds_dwordx4 v[220:221], off
	s_mov_b32 m0, s47
	s_nop 0
	global_load_lds_dwordx4 v[222:223], off
	s_waitcnt vmcnt(8)
	s_waitcnt lgkmcnt(0)
	s_barrier
	s_setprio 1
	s_waitcnt lgkmcnt(0)
	v_mfma_f32_16x16x32_bf16 v[92:95], v[128:131], v[188:191], v[92:95]
	v_mfma_f32_16x16x32_bf16 v[88:91], v[152:155], v[188:191], v[88:91]
	v_mfma_f32_16x16x32_bf16 v[84:87], v[128:131], v[196:199], v[84:87]
	v_mfma_f32_16x16x32_bf16 v[80:83], v[152:155], v[196:199], v[80:83]
	v_mfma_f32_16x16x32_bf16 v[76:79], v[128:131], v[204:207], v[76:79]
	v_mfma_f32_16x16x32_bf16 v[72:75], v[152:155], v[204:207], v[72:75]
	v_mfma_f32_16x16x32_bf16 v[60:63], v[128:131], v[212:215], v[60:63]
	v_mfma_f32_16x16x32_bf16 v[56:59], v[152:155], v[212:215], v[56:59]
	v_mfma_f32_16x16x32_bf16 v[92:95], v[132:135], v[192:195], v[92:95]
	v_mfma_f32_16x16x32_bf16 v[88:91], v[156:159], v[192:195], v[88:91]
	v_mfma_f32_16x16x32_bf16 v[84:87], v[132:135], v[200:203], v[84:87]
	v_mfma_f32_16x16x32_bf16 v[80:83], v[156:159], v[200:203], v[80:83]
	v_mfma_f32_16x16x32_bf16 v[76:79], v[132:135], v[208:211], v[76:79]
	v_mfma_f32_16x16x32_bf16 v[72:75], v[156:159], v[208:211], v[72:75]
	v_mfma_f32_16x16x32_bf16 v[60:63], v[132:135], v[216:219], v[60:63]
	v_mfma_f32_16x16x32_bf16 v[56:59], v[156:159], v[216:219], v[56:59]
	s_setprio 0
	s_setprio 1
	v_mfma_f32_16x16x32_bf16 v[28:31], v[168:171], v[188:191], v[28:31]
	v_mfma_f32_16x16x32_bf16 v[24:27], v[176:179], v[188:191], v[24:27]
	v_mfma_f32_16x16x32_bf16 v[20:23], v[168:171], v[196:199], v[20:23]
	v_mfma_f32_16x16x32_bf16 v[16:19], v[176:179], v[196:199], v[16:19]
	v_mfma_f32_16x16x32_bf16 v[12:15], v[168:171], v[204:207], v[12:15]
	v_mfma_f32_16x16x32_bf16 v[8:11], v[176:179], v[204:207], v[8:11]
	v_mfma_f32_16x16x32_bf16 v[4:7], v[168:171], v[212:215], v[4:7]
	v_mfma_f32_16x16x32_bf16 v[0:3], v[176:179], v[212:215], v[0:3]
	v_mfma_f32_16x16x32_bf16 v[28:31], v[172:175], v[192:195], v[28:31]
	v_mfma_f32_16x16x32_bf16 v[24:27], v[180:183], v[192:195], v[24:27]
	v_mfma_f32_16x16x32_bf16 v[20:23], v[172:175], v[200:203], v[20:23]
	v_mfma_f32_16x16x32_bf16 v[16:19], v[180:183], v[200:203], v[16:19]
	v_mfma_f32_16x16x32_bf16 v[12:15], v[172:175], v[208:211], v[12:15]
	v_mfma_f32_16x16x32_bf16 v[8:11], v[180:183], v[208:211], v[8:11]
	v_mfma_f32_16x16x32_bf16 v[4:7], v[172:175], v[216:219], v[4:7]
	v_mfma_f32_16x16x32_bf16 v[0:3], v[180:183], v[216:219], v[0:3]
	s_setprio 0
	s_barrier
	s_add_i32 s61, 0, 0x18000
	s_add_i32 s62, 0, 0x1c000
	v_add_u32_e32 v156, s61, v163
	v_add_u32_e32 v180, s62, v163
	ds_read_b128 v[128:131], v156
	ds_read_b128 v[132:135], v156 offset:1024
	ds_read_b128 v[152:155], v156 offset:2048
	ds_read_b128 v[156:159], v156 offset:3072
	ds_read_b128 v[168:171], v180
	ds_read_b128 v[172:175], v180 offset:1024
	ds_read_b128 v[176:179], v180 offset:2048
	ds_read_b128 v[180:183], v180 offset:3072
	s_mov_b32 m0, s48
	v_lshl_add_u64 v[224:225], s[40:41], 0, v[144:145]
	ds_read_b128 v[188:191], v167 offset:32768
	ds_read_b128 v[192:195], v167 offset:33792
	ds_read_b128 v[196:199], v167 offset:34816
	ds_read_b128 v[200:203], v167 offset:35840
	ds_read_b128 v[204:207], v167 offset:36864
	ds_read_b128 v[208:211], v167 offset:37888
	ds_read_b128 v[212:215], v167 offset:38912
	ds_read_b128 v[216:219], v167 offset:39936
	global_load_lds_dwordx4 v[224:225], off
	v_lshl_add_u64 v[224:225], s[40:41], 0, v[138:139]
	s_mov_b32 m0, s49
	s_nop 0
	global_load_lds_dwordx4 v[224:225], off
	s_waitcnt vmcnt(8)
	s_waitcnt lgkmcnt(0)
	s_barrier
	s_setprio 1
	s_waitcnt lgkmcnt(0)
	v_mfma_f32_16x16x32_bf16 v[124:127], v[128:131], v[188:191], v[124:127]
	v_mfma_f32_16x16x32_bf16 v[120:123], v[152:155], v[188:191], v[120:123]
	v_mfma_f32_16x16x32_bf16 v[116:119], v[128:131], v[196:199], v[116:119]
	v_mfma_f32_16x16x32_bf16 v[112:115], v[152:155], v[196:199], v[112:115]
	v_mfma_f32_16x16x32_bf16 v[108:111], v[128:131], v[204:207], v[108:111]
	v_mfma_f32_16x16x32_bf16 v[104:107], v[152:155], v[204:207], v[104:107]
	v_mfma_f32_16x16x32_bf16 v[100:103], v[128:131], v[212:215], v[100:103]
	v_mfma_f32_16x16x32_bf16 v[96:99], v[152:155], v[212:215], v[96:99]
	v_mfma_f32_16x16x32_bf16 v[124:127], v[132:135], v[192:195], v[124:127]
	v_mfma_f32_16x16x32_bf16 v[120:123], v[156:159], v[192:195], v[120:123]
	v_mfma_f32_16x16x32_bf16 v[116:119], v[132:135], v[200:203], v[116:119]
	v_mfma_f32_16x16x32_bf16 v[112:115], v[156:159], v[200:203], v[112:115]
	v_mfma_f32_16x16x32_bf16 v[108:111], v[132:135], v[208:211], v[108:111]
	v_mfma_f32_16x16x32_bf16 v[104:107], v[156:159], v[208:211], v[104:107]
	v_mfma_f32_16x16x32_bf16 v[100:103], v[132:135], v[216:219], v[100:103]
	v_mfma_f32_16x16x32_bf16 v[96:99], v[156:159], v[216:219], v[96:99]
	s_setprio 0
	s_setprio 1
	v_mfma_f32_16x16x32_bf16 v[68:71], v[168:171], v[188:191], v[68:71]
	v_mfma_f32_16x16x32_bf16 v[64:67], v[176:179], v[188:191], v[64:67]
	v_mfma_f32_16x16x32_bf16 v[52:55], v[168:171], v[196:199], v[52:55]
	v_mfma_f32_16x16x32_bf16 v[48:51], v[176:179], v[196:199], v[48:51]
	v_mfma_f32_16x16x32_bf16 v[44:47], v[168:171], v[204:207], v[44:47]
	v_mfma_f32_16x16x32_bf16 v[40:43], v[176:179], v[204:207], v[40:43]
	v_mfma_f32_16x16x32_bf16 v[36:39], v[168:171], v[212:215], v[36:39]
	v_mfma_f32_16x16x32_bf16 v[32:35], v[176:179], v[212:215], v[32:35]
	v_mfma_f32_16x16x32_bf16 v[68:71], v[172:175], v[192:195], v[68:71]
	v_mfma_f32_16x16x32_bf16 v[64:67], v[180:183], v[192:195], v[64:67]
	v_mfma_f32_16x16x32_bf16 v[52:55], v[172:175], v[200:203], v[52:55]
	v_mfma_f32_16x16x32_bf16 v[48:51], v[180:183], v[200:203], v[48:51]
	v_mfma_f32_16x16x32_bf16 v[44:47], v[172:175], v[208:211], v[44:47]
	v_mfma_f32_16x16x32_bf16 v[40:43], v[180:183], v[208:211], v[40:43]
	v_mfma_f32_16x16x32_bf16 v[36:39], v[172:175], v[216:219], v[36:39]
	v_mfma_f32_16x16x32_bf16 v[32:35], v[180:183], v[216:219], v[32:35]
	s_setprio 0
	s_barrier
	s_add_i32 s40, s61, s45
	v_lshl_add_u64 v[160:161], v[160:161], 0, s[8:9]
	s_mov_b32 m0, s40
	ds_read_b128 v[188:191], v167 offset:49152
	ds_read_b128 v[192:195], v167 offset:50176
	ds_read_b128 v[196:199], v167 offset:51200
	ds_read_b128 v[200:203], v167 offset:52224
	ds_read_b128 v[204:207], v167 offset:53248
	ds_read_b128 v[208:211], v167 offset:54272
	ds_read_b128 v[212:215], v167 offset:55296
	ds_read_b128 v[216:219], v167 offset:56320
	global_load_lds_dwordx4 v[160:161], off
	s_add_i32 m0, s40, 0x2000
	s_add_u32 s38, s38, 0x40080
	v_lshl_add_u64 v[160:161], v[184:185], 0, s[8:9]
	s_addc_u32 s39, s39, 0
	s_add_i32 s40, s62, s45
	global_load_lds_dwordx4 v[160:161], off
	v_lshl_add_u64 v[160:161], s[38:39], 0, v[146:147]
	s_mov_b32 m0, s40
	s_nop 0
	global_load_lds_dwordx4 v[160:161], off
	v_lshl_add_u64 v[160:161], s[38:39], 0, v[140:141]
	s_add_i32 m0, s40, 0x2000
	s_nop 0
	global_load_lds_dwordx4 v[160:161], off
	v_lshl_add_u64 v[160:161], v[220:221], 0, s[8:9]
	s_mov_b32 m0, s51
	s_nop 0
	global_load_lds_dwordx4 v[160:161], off
	v_lshl_add_u64 v[160:161], v[222:223], 0, s[8:9]
	s_mov_b32 m0, s53
	s_nop 0
	global_load_lds_dwordx4 v[160:161], off
	s_waitcnt vmcnt(8)
	s_waitcnt lgkmcnt(0)
	s_barrier
	s_setprio 1
	s_waitcnt lgkmcnt(0)
	v_mfma_f32_16x16x32_bf16 v[92:95], v[128:131], v[188:191], v[92:95]
	v_mfma_f32_16x16x32_bf16 v[88:91], v[152:155], v[188:191], v[88:91]
	v_mfma_f32_16x16x32_bf16 v[84:87], v[128:131], v[196:199], v[84:87]
	v_mfma_f32_16x16x32_bf16 v[80:83], v[152:155], v[196:199], v[80:83]
	v_mfma_f32_16x16x32_bf16 v[76:79], v[128:131], v[204:207], v[76:79]
	v_mfma_f32_16x16x32_bf16 v[72:75], v[152:155], v[204:207], v[72:75]
	v_mfma_f32_16x16x32_bf16 v[60:63], v[128:131], v[212:215], v[60:63]
	v_mfma_f32_16x16x32_bf16 v[56:59], v[152:155], v[212:215], v[56:59]
	v_mfma_f32_16x16x32_bf16 v[92:95], v[132:135], v[192:195], v[92:95]
	v_mfma_f32_16x16x32_bf16 v[88:91], v[156:159], v[192:195], v[88:91]
	v_mfma_f32_16x16x32_bf16 v[84:87], v[132:135], v[200:203], v[84:87]
	v_mfma_f32_16x16x32_bf16 v[80:83], v[156:159], v[200:203], v[80:83]
	v_mfma_f32_16x16x32_bf16 v[76:79], v[132:135], v[208:211], v[76:79]
	v_mfma_f32_16x16x32_bf16 v[72:75], v[156:159], v[208:211], v[72:75]
	v_mfma_f32_16x16x32_bf16 v[60:63], v[132:135], v[216:219], v[60:63]
	v_mfma_f32_16x16x32_bf16 v[56:59], v[156:159], v[216:219], v[56:59]
	s_setprio 0
	s_setprio 1
	v_mfma_f32_16x16x32_bf16 v[28:31], v[168:171], v[188:191], v[28:31]
	v_mfma_f32_16x16x32_bf16 v[24:27], v[176:179], v[188:191], v[24:27]
	v_mfma_f32_16x16x32_bf16 v[20:23], v[168:171], v[196:199], v[20:23]
	v_mfma_f32_16x16x32_bf16 v[16:19], v[176:179], v[196:199], v[16:19]
	v_mfma_f32_16x16x32_bf16 v[12:15], v[168:171], v[204:207], v[12:15]
	v_mfma_f32_16x16x32_bf16 v[8:11], v[176:179], v[204:207], v[8:11]
	v_mfma_f32_16x16x32_bf16 v[4:7], v[168:171], v[212:215], v[4:7]
	v_mfma_f32_16x16x32_bf16 v[0:3], v[176:179], v[212:215], v[0:3]
	v_mfma_f32_16x16x32_bf16 v[28:31], v[172:175], v[192:195], v[28:31]
	v_mfma_f32_16x16x32_bf16 v[24:27], v[180:183], v[192:195], v[24:27]
	v_mfma_f32_16x16x32_bf16 v[20:23], v[172:175], v[200:203], v[20:23]
	v_mfma_f32_16x16x32_bf16 v[16:19], v[180:183], v[200:203], v[16:19]
	v_mfma_f32_16x16x32_bf16 v[12:15], v[172:175], v[208:211], v[12:15]
	v_mfma_f32_16x16x32_bf16 v[8:11], v[180:183], v[208:211], v[8:11]
	v_mfma_f32_16x16x32_bf16 v[4:7], v[172:175], v[216:219], v[4:7]
	v_mfma_f32_16x16x32_bf16 v[0:3], v[180:183], v[216:219], v[0:3]
	s_setprio 0
	s_barrier
	s_add_i32 s60, s60, 2
	s_add_u32 s36, s36, 0x100
	s_addc_u32 s37, s37, 0
	s_add_u32 s58, s58, 0x100
	s_addc_u32 s59, s59, 0
	s_cmp_gt_u32 s60, 13
	s_cbranch_scc0 .LBB0_566
	s_and_b64 vcc, exec, s[10:11]
	s_cbranch_vccz .LBB0_569
	s_barrier
